# first two DMA waits of each unit's first K-trip leave the previous epilogue's stores outstanding (vmcnt 8+S); phase prologue drains its loads before the first unit
# baseline (speedup 1.0000x reference)
; __host__ __device__ __forceinline__ int perm_a64(int r) { return (r & ~63) + 4 * (r & 15) + ((r >> 4) & 3); }
; #define PG8_WAIT_V(n) asm volatile("s_waitcnt vmcnt(" #n ")" ::: "memory")
; #define PG8_BAR __builtin_amdgcn_s_barrier()
; template <class Epi, class Sched, class Prob>
; __device__ __forceinline__ void gemm_phase(LAS unsigned char* lds, LAS unsigned char* lds_epi, const Prob g, const Sched& S, const Epi& E, int wid) {
;     const int lane = (int)__builtin_amdgcn_mbcnt_hi(~0u, __builtin_amdgcn_mbcnt_lo(~0u, 0u)), tid = wid * 64 + lane, wr = wid >> 2, wc = wid & 3, fr = lane & 15, fq = lane >> 4;
;     const int nt = g.nt;
;     int R0, C0, R1, C1; stage_rc(tid * 16, R0, C0); stage_rc(tid * 16 + 8192, R1, C1);
;     const unsigned lda2 = g.lda, ldb2 = g.ldb;
;     const int Rb0 = Epi::PERM ? ((R0 & ~31) + perm32(R0 & 31)) : R0, Rb1 = Epi::PERM ? ((R1 & ~31) + perm32(R1 & 31)) : R1;
;     const unsigned vB0 = (unsigned)Rb0 * ldb2 + (unsigned)C0 * 2u, vB1 = (unsigned)Rb1 * ldb2 + (unsigned)C1 * 2u;
;     const unsigned hstepB = (unsigned)HALF * ldb2;
;     const size_t kstep = (size_t)(BK * 2);
;     const unsigned ldsw = (unsigned)wid * 1024u;
;     const int aoff = lds_byte(wr * 64 + fr, fq * 8), boff = lds_byte(wc * 32 + fr, fq * 8);
;     ...
;     Unit cur, nxt; int ui = 0; int epi_pm = -1;
;     if (!S.next(0, cur)) return;
;     const int Ra0 = aperm_of<Epi>::v ? perm_a64(R0) : R0, Ra1 = aperm_of<Epi>::v ? perm_a64(R1) : R1;
;     const unsigned cA00 = (unsigned)Ra0 * lda2 + (unsigned)C0 * 2u, cA01 = (unsigned)Ra1 * lda2 + (unsigned)C1 * 2u, cA10 = cA00 + (unsigned)HALF * lda2, cA11 = cA01 + (unsigned)HALF * lda2;
;     f32x4 acc[2][2][4][2];
;     ...
;     PG8_ACC_INIT(cur);
;     bf16x8 At[4][2], B0[2][2], B1[2][2];
;     const char* cA = g.a_base(cur); const char* cB = g.b_base(cur);
;     PG8_STAGE(PG8_SB(0, 0), cB, vB0, vB1); PG8_STAGE(PG8_SB(0, 1), cB + hstepB, vB0, vB1); PG8_STAGE(PG8_SA(0, 0), cA, cA00, cA01); PG8_STAGE(PG8_SA(0, 1), cA, cA10, cA11);
;     if (wr == 1) PG8_BAR;
;     PG8_WAIT_V(2); PG8_BAR;
;     PG8_STAGE(PG8_SB(1, 0), cB + kstep, vB0, vB1); PG8_STAGE(PG8_SA(1, 0), cA + kstep, cA00, cA01); PG8_STAGE(PG8_SB(1, 1), cB + hstepB + kstep, vB0, vB1);
;     PG8_WAIT_V(6); PG8_BAR;
.LBB0_255:
	v_and_b32_e32 v192, 15, v12
	v_readlane_b32 s6, v254, 16
	s_waitcnt vmcnt(0)
	v_and_b32_e32 v19, 48, v12
	s_add_u32 s18, s26, 0x41000000
	v_or_b32_e32 v193, s6, v192
	v_lshlrev_b32_e32 v17, 6, v193
	s_movk_i32 s6, 0x3c0
	v_and_or_b32 v17, v17, s6, v19
	v_readlane_b32 s30, v254, 24
	v_readlane_b32 s6, v254, 31
	s_addc_u32 s19, s27, 0
	v_readlane_b32 s11, v254, 17
	s_and_b32 s6, s6, 0xffffff00
	s_add_i32 s8, 0, 0x20000
	s_add_i32 s7, 0, 0x20400
	s_lshl_b32 s10, s30, 11
	s_add_i32 s9, s8, s6
	s_lshl_b32 s6, s11, 2
	s_add_i32 s61, s7, s10
	s_add_i32 s69, s10, 0
	s_add_i32 s62, s61, s6
	s_add_i32 s63, s69, 0x20600
	s_add_i32 s64, s69, 0x20800
	s_add_i32 s65, s69, 0x20a00
	s_add_i32 s66, s69, 0x21400
	s_add_i32 s67, s69, 0x21600
	s_add_i32 s68, s69, 0x21800
	s_add_i32 s69, s69, 0x21a00
	s_cmp_eq_u32 s11, 0
	s_mov_b64 s[20:21], 0x80
	s_cselect_b64 s[28:29], -1, 0
	s_lshl_b32 s6, s11, 8
	v_lshl_add_u64 v[4:5], v[4:5], 0, s[20:21]
	s_add_i32 m0, s25, 0x18000
	s_add_i32 s44, s7, s6
	s_waitcnt vmcnt(2)
	s_barrier
	global_load_lds_dwordx4 v[4:5], off
	v_lshl_add_u64 v[2:3], v[2:3], 0, s[20:21]
	s_add_i32 m0, s25, 0x1a000
	s_add_i32 s70, s25, 0x8000
	s_add_i32 s71, s25, 0xa000
	global_load_lds_dwordx4 v[2:3], off
	v_lshl_add_u64 v[0:1], v[0:1], 0, s[20:21]
	s_mov_b32 m0, s70
	s_add_u32 s6, s52, 0x80080
	global_load_lds_dwordx4 v[0:1], off
	v_lshl_add_u64 v[0:1], v[6:7], 0, s[20:21]
	s_mov_b32 m0, s71
	s_addc_u32 s7, s53, 0
	global_load_lds_dwordx4 v[0:1], off
	v_lshl_add_u64 v[0:1], s[6:7], 0, v[144:145]
	s_add_i32 m0, s25, 0x1c000
	v_and_b32_e32 v3, 0xffffffc0, v12
	global_load_lds_dwordx4 v[0:1], off
	v_lshl_add_u64 v[0:1], s[6:7], 0, v[146:147]
	s_add_i32 m0, s25, 0x1e000
	v_xor_b32_e32 v2, 16, v12
	global_load_lds_dwordx4 v[0:1], off
	v_add_u32_e32 v3, 64, v3
	v_cmp_lt_i32_e32 vcc, v2, v3
	v_add_u32_e32 v0, s91, v12
	v_and_b32_e32 v15, 0xfffffc00, v15
	v_cndmask_b32_e32 v2, v12, v2, vcc
	v_lshlrev_b32_e32 v197, 2, v2
	v_xor_b32_e32 v2, 32, v12
	v_cmp_lt_i32_e32 vcc, v2, v3
	v_lshlrev_b32_e32 v21, 2, v193
	s_movk_i32 s6, 0x100
	v_cndmask_b32_e32 v2, v12, v2, vcc
	v_lshlrev_b32_e32 v198, 2, v2
	v_xor_b32_e32 v2, 1, v12
	v_cmp_lt_i32_e32 vcc, v2, v3
	v_ashrrev_i32_e32 v1, 31, v0
	v_readlane_b32 s12, v254, 25
	v_cndmask_b32_e32 v2, v12, v2, vcc
	v_lshlrev_b32_e32 v200, 2, v2
	v_xor_b32_e32 v2, 2, v12
	v_cmp_lt_i32_e32 vcc, v2, v3
	v_lshl_add_u32 v20, s30, 13, v15
	v_and_b32_e32 v21, 32, v21
	v_cndmask_b32_e32 v2, v12, v2, vcc
	v_lshlrev_b32_e32 v201, 2, v2
	v_xor_b32_e32 v2, 4, v12
	v_cmp_lt_i32_e32 vcc, v2, v3
	v_cmp_gt_i32_e64 s[6:7], s6, v0
	v_lshl_add_u32 v195, v0, 2, s8
	v_cndmask_b32_e32 v2, v12, v2, vcc
	v_lshlrev_b32_e32 v202, 2, v2
	v_xor_b32_e32 v2, 8, v12
	v_cmp_lt_i32_e32 vcc, v2, v3
	v_readlane_b32 s13, v254, 26
	v_or_b32_e32 v3, s30, v192
	v_cndmask_b32_e32 v2, v12, v2, vcc
	v_cmp_eq_u32_e32 vcc, 0, v192
	v_readlane_b32 s34, v254, 19
	v_lshl_add_u64 v[0:1], v[0:1], 2, s[26:27]
	s_mov_b64 s[30:31], 0x100000
	v_ashrrev_i32_e32 v18, 4, v12
	v_bitop3_b32 v20, v17, v20, v21 bitop3:0xde
	v_lshl_or_b32 v17, v192, 6, v19
	v_lshlrev_b32_e32 v19, 2, v192
	s_and_b64 s[22:23], s[12:13], vcc
	v_lshl_add_u64 v[160:161], v[0:1], 0, s[30:31]
	s_lshl_b32 s30, s34, 2
	v_lshlrev_b32_e32 v16, 3, v18
	v_lshl_add_u32 v15, s11, 12, v15
	v_and_b32_e32 v21, 32, v19
	s_add_u32 s30, s26, s30
	v_bitop3_b32 v194, v17, v15, v21 bitop3:0xde
	v_ashrrev_i32_e32 v17, 31, v16
	s_addc_u32 s31, s27, 0
	v_lshl_add_u64 v[0:1], v[16:17], 2, s[30:31]
	s_mov_b64 s[30:31], 0x3dc400
	v_lshl_add_u64 v[162:163], v[0:1], 0, s[30:31]
	s_mov_b64 s[30:31], 0x290000
	v_lshl_add_u64 v[164:165], v[0:1], 0, s[30:31]
	v_lshlrev_b32_e32 v0, 5, v18
	v_and_b32_e32 v156, 32, v0
	v_lshl_add_u64 v[0:1], s[26:27], 0, v[156:157]
	s_mov_b64 s[26:27], 0x2d0000
	v_lshl_add_u64 v[166:167], v[0:1], 0, s[26:27]
	v_lshlrev_b32_e32 v0, 15, v11
	v_and_b32_e32 v0, 0xffff0000, v0
	v_lshl_add_u32 v0, v13, 12, v0
	v_and_b32_e32 v1, 1, v11
	v_lshl_or_b32 v0, v1, 6, v0
	v_lshlrev_b32_e32 v1, 1, v14
	v_add3_u32 v168, v0, v1, s3
	v_lshlrev_b32_e32 v0, 15, v8
	v_and_b32_e32 v0, 0xffff0000, v0
	s_waitcnt vmcnt(0)
	v_lshl_add_u32 v0, v9, 12, v0
	v_and_b32_e32 v1, 1, v8
	v_lshlrev_b32_e32 v203, 2, v2
	v_lshlrev_b32_e32 v2, 6, v18
	v_readlane_b32 s35, v254, 20
	v_lshl_or_b32 v0, v1, 6, v0
	v_lshlrev_b32_e32 v1, 1, v10
	v_mov_b32_e32 v151, v157
	v_mov_b32_e32 v155, v157
	v_add_u32_e32 v196, s9, v19
	v_cmp_gt_u32_e64 s[8:9], 16, v12
	v_lshlrev_b32_e32 v199, 5, v192
	v_cmp_lt_i32_e64 s[10:11], 1, v18
	v_cmp_eq_u32_e64 s[12:13], 0, v3
	v_lshl_add_u64 v[158:159], v[16:17], 0, s[34:35]
	v_mov_b32_e32 v169, v157
	v_add3_u32 v170, v0, v1, s3
	v_mov_b32_e32 v171, v157
	s_add_i32 s72, 0, 0x10000
	s_add_i32 s73, 0, 0x14000
	v_add_u32_e32 v204, 0, v20
	v_mov_b32_e32 v205, 0x358637bd
	s_mov_b32 s74, 0xf800000
	v_mov_b32_e32 v206, 0x260
	s_xor_b64 s[26:27], s[28:29], -1
	s_mov_b64 s[28:29], 0x40000
	s_mov_b64 s[30:31], 0x40400
	s_mov_b64 s[34:35], 0x40800
	s_mov_b64 s[36:37], 0x40c00
	s_mov_b32 s38, 0x3b800000
	s_mov_b64 s[40:41], 0x18000
	s_mov_b64 s[42:43], 0x78000
	v_mov_b64_e32 v[172:173], 0x5ff
	v_add_u32_e32 v207, s44, v2
	s_mov_b32 s75, 0
	s_barrier
	s_branch .LBB0_258

; #define PG8_STAGE(bufoff, gbase, o0, o1) do { \
;         __builtin_amdgcn_global_load_lds((const unsigned*)((const char*)(gbase) + (o0)), (LAS unsigned*)(lds + (bufoff) + ldsw), 16, 0, 0); \
;         __builtin_amdgcn_global_load_lds((const unsigned*)((const char*)(gbase) + (o1)), (LAS unsigned*)(lds + (bufoff) + ldsw + 8192), 16, 0, 0); } while (0)
; #define PG8_LDA(dst, b, h) do { _Pragma("unroll") for (int m = 0; m < 4; ++m) _Pragma("unroll") for (int k = 0; k < 2; ++k) dst[m][k] = *(const LAS bf16x8*)(lds + PG8_SA(b, h) + aoff + m * 2048 + k * 1024); } while (0)
; #define PG8_LDB(dst, b, h) do { _Pragma("unroll") for (int n = 0; n < 2; ++n) _Pragma("unroll") for (int k = 0; k < 2; ++k) dst[n][k] = *(const LAS bf16x8*)(lds + PG8_SB(b, h) + boff + n * 2048 + k * 1024); } while (0)
; #define PG8_WAIT_V(n) asm volatile("s_waitcnt vmcnt(" #n ")" ::: "memory")
; #define PG8_WAIT_L(n) asm volatile("s_waitcnt lgkmcnt(" #n ")" ::: "memory")
; #define PG8_BAR __builtin_amdgcn_s_barrier()
; #define PG8_SCHED __builtin_amdgcn_sched_barrier(0)
; template <class Epi, class Sched, class Prob>
; __device__ __forceinline__ void gemm_phase(LAS unsigned char* lds, LAS unsigned char* lds_epi, const Prob g, const Sched& S, const Epi& E, int wid) {
;     ...
;         for (int t = 0; t < nt; t += 2) {
;             const bool last = (t == nt - 2);
;             const char* a1 = cA + (size_t)(t + 1) * kstep;
;             const char* a2 = last ? nA : cA + (size_t)(t + 2) * kstep; const char* b2 = last ? nB : cB + (size_t)(t + 2) * kstep;
;             const char* a3 = a2 + kstep; const char* b3 = b2 + kstep;
;             PG8_LDB(B0, 0, 0); PG8_LDB(B1, 0, 1); PG8_SCHED; PG8_LDA(At, 0, 0); PG8_STAGE(PG8_SA(1, 1), a1, cA10, cA11);
;             PG8_WAIT_V(8); PG8_WAIT_L(0); PG8_BAR; PG8_MMA(0, 0, At, B0); PG8_MMA(0, 1, At, B1); PG8_BAR; PG8_SCHED;
;             PG8_LDA(At, 0, 1); PG8_STAGE(PG8_SB(0, 0), b2, vB0, vB1); PG8_STAGE(PG8_SB(0, 1), b2 + hstepB, vB0, vB1); PG8_STAGE(PG8_SA(0, 0), a2, cA00, cA01);
.LBB0_261:
	s_ashr_i32 s3, s2, 31
	s_lshl_b64 s[48:49], s[2:3], 20
	s_add_u32 s48, s33, s48
	s_addc_u32 s49, s39, s49
	s_and_b64 s[50:51], s[46:47], exec
	s_cselect_b32 s3, s49, s15
	s_cselect_b32 s77, s48, s14
	s_ashr_i32 s45, s44, 31
	s_lshl_b64 s[50:51], s[44:45], 20
	s_add_u32 s50, s56, s50
	s_addc_u32 s51, s57, s51
	s_and_b64 s[54:55], s[46:47], exec
	s_cselect_b32 s45, s51, s53
	s_cselect_b32 s78, s50, s52
	s_add_u32 s14, s14, 0x80
	s_addc_u32 s15, s15, 0
	s_add_u32 s79, s52, 0x100
	v_mov_b32_e32 v44, 0
	s_addc_u32 s80, s53, 0
	s_mov_b32 s81, -2
	v_add_u32_e32 v140, s72, v194
	v_add_u32_e32 v156, s73, v194
	ds_read_b128 v[128:131], v140
	ds_read_b128 v[132:135], v140 offset:1024
	ds_read_b128 v[136:139], v140 offset:2048
	ds_read_b128 v[140:143], v140 offset:3072
	ds_read_b128 v[174:177], v156
	ds_read_b128 v[178:181], v156 offset:1024
	ds_read_b128 v[182:185], v156 offset:2048
	ds_read_b128 v[186:189], v156 offset:3072
	s_add_u32 s52, s14, 0x80
	s_addc_u32 s53, s15, 0
	s_cmp_eq_u32 s81, 28
	s_cselect_b32 s55, s3, s53
	s_cselect_b32 s54, s77, s52
	s_cselect_b32 s53, s45, s80
	s_cselect_b32 s52, s78, s79
	v_lshl_add_u64 v[190:191], s[14:15], 0, v[170:171]
	s_add_i32 m0, s25, 0xc000
	ds_read_b128 v[208:211], v204
	ds_read_b128 v[212:215], v204 offset:1024
	ds_read_b128 v[216:219], v204 offset:2048
	ds_read_b128 v[220:223], v204 offset:3072
	ds_read_b128 v[224:227], v204 offset:4096
	ds_read_b128 v[228:231], v204 offset:5120
	ds_read_b128 v[232:235], v204 offset:6144
	ds_read_b128 v[238:241], v204 offset:7168
	global_load_lds_dwordx4 v[190:191], off
	v_lshl_add_u64 v[190:191], s[14:15], 0, v[168:169]
	s_add_i32 m0, s25, 0xe000
	s_nop 0
	global_load_lds_dwordx4 v[190:191], off
	s_waitcnt vmcnt(24)
	s_waitcnt lgkmcnt(0)
	s_barrier
	s_setprio 1
	s_waitcnt lgkmcnt(0)
	v_mfma_f32_16x16x32_bf16 v[80:83], v[128:131], v[208:211], 0
	v_mfma_f32_16x16x32_bf16 v[92:95], v[136:139], v[208:211], 0
	v_mfma_f32_16x16x32_bf16 v[52:55], v[128:131], v[216:219], 0
	v_mfma_f32_16x16x32_bf16 v[68:71], v[136:139], v[216:219], 0
	v_mfma_f32_16x16x32_bf16 v[28:31], v[128:131], v[224:227], 0
	v_mfma_f32_16x16x32_bf16 v[36:39], v[136:139], v[224:227], 0
	v_mfma_f32_16x16x32_bf16 v[8:11], v[128:131], v[232:235], 0
	v_mfma_f32_16x16x32_bf16 v[16:19], v[136:139], v[232:235], 0
	v_mfma_f32_16x16x32_bf16 v[80:83], v[132:135], v[212:215], v[80:83]
	v_mfma_f32_16x16x32_bf16 v[92:95], v[140:143], v[212:215], v[92:95]
	v_mfma_f32_16x16x32_bf16 v[52:55], v[132:135], v[220:223], v[52:55]
	v_mfma_f32_16x16x32_bf16 v[68:71], v[140:143], v[220:223], v[68:71]
	v_mfma_f32_16x16x32_bf16 v[28:31], v[132:135], v[228:231], v[28:31]
	v_mfma_f32_16x16x32_bf16 v[36:39], v[140:143], v[228:231], v[36:39]
	v_mfma_f32_16x16x32_bf16 v[8:11], v[132:135], v[238:241], v[8:11]
	v_mfma_f32_16x16x32_bf16 v[16:19], v[140:143], v[238:241], v[16:19]
	s_setprio 0
	s_setprio 1
	v_mfma_f32_16x16x32_bf16 v[120:123], v[174:177], v[208:211], 0
	v_mfma_f32_16x16x32_bf16 v[124:127], v[182:185], v[208:211], 0
	v_mfma_f32_16x16x32_bf16 v[104:107], v[174:177], v[216:219], 0
	v_mfma_f32_16x16x32_bf16 v[112:115], v[182:185], v[216:219], 0
	v_mfma_f32_16x16x32_bf16 v[84:87], v[174:177], v[224:227], 0
	v_mfma_f32_16x16x32_bf16 v[96:99], v[182:185], v[224:227], 0
	v_mfma_f32_16x16x32_bf16 v[48:51], v[174:177], v[232:235], 0
	v_mfma_f32_16x16x32_bf16 v[64:67], v[182:185], v[232:235], 0
	v_mfma_f32_16x16x32_bf16 v[120:123], v[178:181], v[212:215], v[120:123]
	v_mfma_f32_16x16x32_bf16 v[124:127], v[186:189], v[212:215], v[124:127]
	v_mfma_f32_16x16x32_bf16 v[104:107], v[178:181], v[220:223], v[104:107]
	v_mfma_f32_16x16x32_bf16 v[112:115], v[186:189], v[220:223], v[112:115]
	v_mfma_f32_16x16x32_bf16 v[84:87], v[178:181], v[228:231], v[84:87]
	v_mfma_f32_16x16x32_bf16 v[96:99], v[186:189], v[228:231], v[96:99]
	v_mfma_f32_16x16x32_bf16 v[48:51], v[178:181], v[238:241], v[48:51]
	v_mfma_f32_16x16x32_bf16 v[64:67], v[186:189], v[238:241], v[64:67]
	s_setprio 0
	s_barrier
	s_add_i32 s82, s72, s97
	v_lshl_add_u64 v[190:191], s[52:53], 0, v[144:145]
	s_mov_b32 m0, s82
	ds_read_b128 v[208:211], v204 offset:16384
	ds_read_b128 v[212:215], v204 offset:17408
	ds_read_b128 v[216:219], v204 offset:18432
	ds_read_b128 v[220:223], v204 offset:19456
	ds_read_b128 v[224:227], v204 offset:20480
	ds_read_b128 v[228:231], v204 offset:21504
	ds_read_b128 v[232:235], v204 offset:22528
	ds_read_b128 v[238:241], v204 offset:23552
	global_load_lds_dwordx4 v[190:191], off
	s_add_i32 m0, s82, 0x2000
	s_add_u32 s82, s52, 0x80000
	v_lshl_add_u64 v[236:237], s[52:53], 0, v[146:147]
	s_addc_u32 s83, s53, 0
	s_add_i32 s84, s73, s97
	global_load_lds_dwordx4 v[236:237], off
	v_lshl_add_u64 v[242:243], s[82:83], 0, v[144:145]
	s_mov_b32 m0, s84
	v_lshl_add_u64 v[244:245], s[54:55], 0, v[152:153]
	global_load_lds_dwordx4 v[242:243], off
	v_lshl_add_u64 v[242:243], s[82:83], 0, v[146:147]
	s_add_i32 m0, s84, 0x2000
	s_nop 0
	global_load_lds_dwordx4 v[242:243], off
	v_lshl_add_u64 v[242:243], s[54:55], 0, v[148:149]
	s_mov_b32 m0, s25
	s_nop 0
	global_load_lds_dwordx4 v[242:243], off
	s_mov_b32 m0, s58
	s_nop 0
	global_load_lds_dwordx4 v[244:245], off
	s_waitcnt vmcnt(24)
	s_waitcnt lgkmcnt(0)
	s_barrier
; #define PG8_STAGE(bufoff, gbase, o0, o1) do { \
;         __builtin_amdgcn_global_load_lds((const unsigned*)((const char*)(gbase) + (o0)), (LAS unsigned*)(lds + (bufoff) + ldsw), 16, 0, 0); \
;         __builtin_amdgcn_global_load_lds((const unsigned*)((const char*)(gbase) + (o1)), (LAS unsigned*)(lds + (bufoff) + ldsw + 8192), 16, 0, 0); } while (0)
; #define PG8_LDA(dst, b, h) do { _Pragma("unroll") for (int m = 0; m < 4; ++m) _Pragma("unroll") for (int k = 0; k < 2; ++k) dst[m][k] = *(const LAS bf16x8*)(lds + PG8_SA(b, h) + aoff + m * 2048 + k * 1024); } while (0)
; #define PG8_LDB(dst, b, h) do { _Pragma("unroll") for (int n = 0; n < 2; ++n) _Pragma("unroll") for (int k = 0; k < 2; ++k) dst[n][k] = *(const LAS bf16x8*)(lds + PG8_SB(b, h) + boff + n * 2048 + k * 1024); } while (0)
; #define PG8_WAIT_V(n) asm volatile("s_waitcnt vmcnt(" #n ")" ::: "memory")
; #define PG8_WAIT_L(n) asm volatile("s_waitcnt lgkmcnt(" #n ")" ::: "memory")
; #define PG8_BAR __builtin_amdgcn_s_barrier()
; #define PG8_SCHED __builtin_amdgcn_sched_barrier(0)
; template <class Epi, class Sched, class Prob>
; __device__ __forceinline__ void gemm_phase(LAS unsigned char* lds, LAS unsigned char* lds_epi, const Prob g, const Sched& S, const Epi& E, int wid) {
;     ...
;             PG8_WAIT_V(8); PG8_WAIT_L(0); PG8_BAR; PG8_MMA(0, 0, At, B0); PG8_MMA(0, 1, At, B1); PG8_BAR; PG8_SCHED;
;             PG8_LDA(At, 0, 1); PG8_STAGE(PG8_SB(0, 0), b2, vB0, vB1); PG8_STAGE(PG8_SB(0, 1), b2 + hstepB, vB0, vB1); PG8_STAGE(PG8_SA(0, 0), a2, cA00, cA01);
;             PG8_WAIT_V(8); PG8_WAIT_L(0); PG8_BAR; PG8_MMA(1, 0, At, B0); PG8_MMA(1, 1, At, B1); PG8_BAR; PG8_SCHED;
;             PG8_LDB(B0, 1, 0); PG8_LDB(B1, 1, 1); PG8_SCHED; PG8_LDA(At, 1, 0); PG8_STAGE(PG8_SA(0, 1), a2, cA10, cA11);
;             PG8_WAIT_V(8); PG8_WAIT_L(0); PG8_BAR; PG8_MMA(0, 0, At, B0); PG8_MMA(0, 1, At, B1); PG8_BAR; PG8_SCHED;
	s_setprio 1
	s_waitcnt lgkmcnt(0)
	v_mfma_f32_16x16x32_bf16 v[56:59], v[128:131], v[208:211], 0
	v_mfma_f32_16x16x32_bf16 v[72:75], v[136:139], v[208:211], 0
	v_mfma_f32_16x16x32_bf16 v[32:35], v[128:131], v[216:219], 0
	v_mfma_f32_16x16x32_bf16 v[40:43], v[136:139], v[216:219], 0
	v_mfma_f32_16x16x32_bf16 v[12:15], v[128:131], v[224:227], 0
	v_mfma_f32_16x16x32_bf16 v[20:23], v[136:139], v[224:227], 0
	v_mfma_f32_16x16x32_bf16 v[0:3], v[128:131], v[232:235], 0
	v_mfma_f32_16x16x32_bf16 v[4:7], v[136:139], v[232:235], 0
	v_mfma_f32_16x16x32_bf16 v[56:59], v[132:135], v[212:215], v[56:59]
	v_mfma_f32_16x16x32_bf16 v[72:75], v[140:143], v[212:215], v[72:75]
	v_mfma_f32_16x16x32_bf16 v[32:35], v[132:135], v[220:223], v[32:35]
	v_mfma_f32_16x16x32_bf16 v[40:43], v[140:143], v[220:223], v[40:43]
	v_mfma_f32_16x16x32_bf16 v[12:15], v[132:135], v[228:231], v[12:15]
	v_mfma_f32_16x16x32_bf16 v[20:23], v[140:143], v[228:231], v[20:23]
	v_mfma_f32_16x16x32_bf16 v[0:3], v[132:135], v[238:241], v[0:3]
	v_mfma_f32_16x16x32_bf16 v[4:7], v[140:143], v[238:241], v[4:7]
	s_setprio 0
	s_setprio 1
	v_mfma_f32_16x16x32_bf16 v[108:111], v[174:177], v[208:211], 0
	v_mfma_f32_16x16x32_bf16 v[116:119], v[182:185], v[208:211], 0
	v_mfma_f32_16x16x32_bf16 v[88:91], v[174:177], v[216:219], 0
	v_mfma_f32_16x16x32_bf16 v[100:103], v[182:185], v[216:219], 0
	v_mfma_f32_16x16x32_bf16 v[60:63], v[174:177], v[224:227], 0
	v_mfma_f32_16x16x32_bf16 v[76:79], v[182:185], v[224:227], 0
	v_mfma_f32_16x16x32_bf16 v[24:27], v[174:177], v[232:235], 0
	v_mfma_f32_16x16x32_bf16 v[44:47], v[182:185], v[232:235], 0
	v_mfma_f32_16x16x32_bf16 v[108:111], v[178:181], v[212:215], v[108:111]
	v_mfma_f32_16x16x32_bf16 v[116:119], v[186:189], v[212:215], v[116:119]
	v_mfma_f32_16x16x32_bf16 v[88:91], v[178:181], v[220:223], v[88:91]
	v_mfma_f32_16x16x32_bf16 v[100:103], v[186:189], v[220:223], v[100:103]
	v_mfma_f32_16x16x32_bf16 v[60:63], v[178:181], v[228:231], v[60:63]
	v_mfma_f32_16x16x32_bf16 v[76:79], v[186:189], v[228:231], v[76:79]
	v_mfma_f32_16x16x32_bf16 v[24:27], v[178:181], v[238:241], v[24:27]
	v_mfma_f32_16x16x32_bf16 v[44:47], v[186:189], v[238:241], v[44:47]
	s_setprio 0
	s_barrier
	s_add_i32 s82, 0, 0x18000
	s_add_i32 s83, 0, 0x1c000
	v_add_u32_e32 v140, s82, v194
	v_add_u32_e32 v156, s83, v194
	ds_read_b128 v[128:131], v140
	ds_read_b128 v[132:135], v140 offset:1024
	ds_read_b128 v[136:139], v140 offset:2048
	ds_read_b128 v[140:143], v140 offset:3072
	ds_read_b128 v[174:177], v156
	ds_read_b128 v[178:181], v156 offset:1024
	ds_read_b128 v[182:185], v156 offset:2048
	ds_read_b128 v[186:189], v156 offset:3072
	s_mov_b32 m0, s59
	v_lshl_add_u64 v[246:247], s[54:55], 0, v[150:151]
	ds_read_b128 v[208:211], v204 offset:32768
	ds_read_b128 v[212:215], v204 offset:33792
	ds_read_b128 v[216:219], v204 offset:34816
	ds_read_b128 v[220:223], v204 offset:35840
	ds_read_b128 v[224:227], v204 offset:36864
	ds_read_b128 v[228:231], v204 offset:37888
	ds_read_b128 v[232:235], v204 offset:38912
	ds_read_b128 v[238:241], v204 offset:39936
	global_load_lds_dwordx4 v[246:247], off
	v_lshl_add_u64 v[246:247], s[54:55], 0, v[154:155]
	s_mov_b32 m0, s60
	s_nop 0
	global_load_lds_dwordx4 v[246:247], off
	s_waitcnt vmcnt(8)
	s_waitcnt lgkmcnt(0)
	s_barrier
	s_setprio 1
	s_waitcnt lgkmcnt(0)
	v_mfma_f32_16x16x32_bf16 v[80:83], v[128:131], v[208:211], v[80:83]
	v_mfma_f32_16x16x32_bf16 v[92:95], v[136:139], v[208:211], v[92:95]
	v_mfma_f32_16x16x32_bf16 v[52:55], v[128:131], v[216:219], v[52:55]
	v_mfma_f32_16x16x32_bf16 v[68:71], v[136:139], v[216:219], v[68:71]
	v_mfma_f32_16x16x32_bf16 v[28:31], v[128:131], v[224:227], v[28:31]
	v_mfma_f32_16x16x32_bf16 v[36:39], v[136:139], v[224:227], v[36:39]
	v_mfma_f32_16x16x32_bf16 v[8:11], v[128:131], v[232:235], v[8:11]
	v_mfma_f32_16x16x32_bf16 v[16:19], v[136:139], v[232:235], v[16:19]
	v_mfma_f32_16x16x32_bf16 v[80:83], v[132:135], v[212:215], v[80:83]
	v_mfma_f32_16x16x32_bf16 v[92:95], v[140:143], v[212:215], v[92:95]
	v_mfma_f32_16x16x32_bf16 v[52:55], v[132:135], v[220:223], v[52:55]
	v_mfma_f32_16x16x32_bf16 v[68:71], v[140:143], v[220:223], v[68:71]
	v_mfma_f32_16x16x32_bf16 v[28:31], v[132:135], v[228:231], v[28:31]
	v_mfma_f32_16x16x32_bf16 v[36:39], v[140:143], v[228:231], v[36:39]
	v_mfma_f32_16x16x32_bf16 v[8:11], v[132:135], v[238:241], v[8:11]
	v_mfma_f32_16x16x32_bf16 v[16:19], v[140:143], v[238:241], v[16:19]
	s_setprio 0
	s_setprio 1
	v_mfma_f32_16x16x32_bf16 v[120:123], v[174:177], v[208:211], v[120:123]
	v_mfma_f32_16x16x32_bf16 v[124:127], v[182:185], v[208:211], v[124:127]
	v_mfma_f32_16x16x32_bf16 v[104:107], v[174:177], v[216:219], v[104:107]
	v_mfma_f32_16x16x32_bf16 v[112:115], v[182:185], v[216:219], v[112:115]
	v_mfma_f32_16x16x32_bf16 v[84:87], v[174:177], v[224:227], v[84:87]
	v_mfma_f32_16x16x32_bf16 v[96:99], v[182:185], v[224:227], v[96:99]
	v_mfma_f32_16x16x32_bf16 v[48:51], v[174:177], v[232:235], v[48:51]
	v_mfma_f32_16x16x32_bf16 v[64:67], v[182:185], v[232:235], v[64:67]
	v_mfma_f32_16x16x32_bf16 v[120:123], v[178:181], v[212:215], v[120:123]
	v_mfma_f32_16x16x32_bf16 v[124:127], v[186:189], v[212:215], v[124:127]
	v_mfma_f32_16x16x32_bf16 v[104:107], v[178:181], v[220:223], v[104:107]
	v_mfma_f32_16x16x32_bf16 v[112:115], v[186:189], v[220:223], v[112:115]
	v_mfma_f32_16x16x32_bf16 v[84:87], v[178:181], v[228:231], v[84:87]
	v_mfma_f32_16x16x32_bf16 v[96:99], v[186:189], v[228:231], v[96:99]
	v_mfma_f32_16x16x32_bf16 v[48:51], v[178:181], v[238:241], v[48:51]
	v_mfma_f32_16x16x32_bf16 v[64:67], v[186:189], v[238:241], v[64:67]
	s_setprio 0
	s_barrier
; #define PG8_STAGE(bufoff, gbase, o0, o1) do { \
;         __builtin_amdgcn_global_load_lds((const unsigned*)((const char*)(gbase) + (o0)), (LAS unsigned*)(lds + (bufoff) + ldsw), 16, 0, 0); \
;         __builtin_amdgcn_global_load_lds((const unsigned*)((const char*)(gbase) + (o1)), (LAS unsigned*)(lds + (bufoff) + ldsw + 8192), 16, 0, 0); } while (0)
; #define PG8_LDA(dst, b, h) do { _Pragma("unroll") for (int m = 0; m < 4; ++m) _Pragma("unroll") for (int k = 0; k < 2; ++k) dst[m][k] = *(const LAS bf16x8*)(lds + PG8_SA(b, h) + aoff + m * 2048 + k * 1024); } while (0)
; #define PG8_LDB(dst, b, h) do { _Pragma("unroll") for (int n = 0; n < 2; ++n) _Pragma("unroll") for (int k = 0; k < 2; ++k) dst[n][k] = *(const LAS bf16x8*)(lds + PG8_SB(b, h) + boff + n * 2048 + k * 1024); } while (0)
; #define PG8_WAIT_V(n) asm volatile("s_waitcnt vmcnt(" #n ")" ::: "memory")
; #define PG8_WAIT_L(n) asm volatile("s_waitcnt lgkmcnt(" #n ")" ::: "memory")
; #define PG8_BAR __builtin_amdgcn_s_barrier()
; #define PG8_SCHED __builtin_amdgcn_sched_barrier(0)
; template <class Epi, class Sched, class Prob>
; __device__ __forceinline__ void gemm_phase(LAS unsigned char* lds, LAS unsigned char* lds_epi, const Prob g, const Sched& S, const Epi& E, int wid) {
;     ...
;             PG8_LDB(B0, 1, 0); PG8_LDB(B1, 1, 1); PG8_SCHED; PG8_LDA(At, 1, 0); PG8_STAGE(PG8_SA(0, 1), a2, cA10, cA11);
;             PG8_WAIT_V(8); PG8_WAIT_L(0); PG8_BAR; PG8_MMA(0, 0, At, B0); PG8_MMA(0, 1, At, B1); PG8_BAR; PG8_SCHED;
;             PG8_LDA(At, 1, 1); PG8_STAGE(PG8_SB(1, 0), b3, vB0, vB1); PG8_STAGE(PG8_SB(1, 1), b3 + hstepB, vB0, vB1); PG8_STAGE(PG8_SA(1, 0), a3, cA00, cA01);
;             PG8_WAIT_V(8); PG8_WAIT_L(0); PG8_BAR; PG8_MMA(1, 0, At, B0); PG8_MMA(1, 1, At, B1); PG8_BAR; PG8_SCHED;
;         }
	s_add_i32 s54, s82, s97
	v_lshl_add_u64 v[190:191], v[190:191], 0, s[20:21]
	s_mov_b32 m0, s54
	ds_read_b128 v[208:211], v204 offset:49152
	ds_read_b128 v[212:215], v204 offset:50176
	ds_read_b128 v[216:219], v204 offset:51200
	ds_read_b128 v[220:223], v204 offset:52224
	ds_read_b128 v[224:227], v204 offset:53248
	ds_read_b128 v[228:231], v204 offset:54272
	ds_read_b128 v[232:235], v204 offset:55296
	ds_read_b128 v[238:241], v204 offset:56320
	global_load_lds_dwordx4 v[190:191], off
	s_add_i32 m0, s54, 0x2000
	s_add_u32 s52, s52, 0x80080
	v_lshl_add_u64 v[190:191], v[236:237], 0, s[20:21]
	s_addc_u32 s53, s53, 0
	s_add_i32 s54, s83, s97
	global_load_lds_dwordx4 v[190:191], off
	v_lshl_add_u64 v[190:191], s[52:53], 0, v[144:145]
	s_mov_b32 m0, s54
	s_nop 0
	global_load_lds_dwordx4 v[190:191], off
	v_lshl_add_u64 v[190:191], s[52:53], 0, v[146:147]
	s_add_i32 m0, s54, 0x2000
	s_nop 0
	global_load_lds_dwordx4 v[190:191], off
	v_lshl_add_u64 v[190:191], v[242:243], 0, s[20:21]
	s_mov_b32 m0, s70
	s_nop 0
	global_load_lds_dwordx4 v[190:191], off
	v_lshl_add_u64 v[190:191], v[244:245], 0, s[20:21]
	s_mov_b32 m0, s71
	s_nop 0
	global_load_lds_dwordx4 v[190:191], off
	s_waitcnt vmcnt(8)
	s_waitcnt lgkmcnt(0)
	s_barrier
	s_setprio 1
	s_waitcnt lgkmcnt(0)
	v_mfma_f32_16x16x32_bf16 v[56:59], v[128:131], v[208:211], v[56:59]
	v_mfma_f32_16x16x32_bf16 v[72:75], v[136:139], v[208:211], v[72:75]
	v_mfma_f32_16x16x32_bf16 v[32:35], v[128:131], v[216:219], v[32:35]
	v_mfma_f32_16x16x32_bf16 v[40:43], v[136:139], v[216:219], v[40:43]
	v_mfma_f32_16x16x32_bf16 v[12:15], v[128:131], v[224:227], v[12:15]
	v_mfma_f32_16x16x32_bf16 v[20:23], v[136:139], v[224:227], v[20:23]
	v_mfma_f32_16x16x32_bf16 v[0:3], v[128:131], v[232:235], v[0:3]
	v_mfma_f32_16x16x32_bf16 v[4:7], v[136:139], v[232:235], v[4:7]
	v_mfma_f32_16x16x32_bf16 v[56:59], v[132:135], v[212:215], v[56:59]
	v_mfma_f32_16x16x32_bf16 v[72:75], v[140:143], v[212:215], v[72:75]
	v_mfma_f32_16x16x32_bf16 v[32:35], v[132:135], v[220:223], v[32:35]
	v_mfma_f32_16x16x32_bf16 v[40:43], v[140:143], v[220:223], v[40:43]
	v_mfma_f32_16x16x32_bf16 v[12:15], v[132:135], v[228:231], v[12:15]
	v_mfma_f32_16x16x32_bf16 v[20:23], v[140:143], v[228:231], v[20:23]
	v_mfma_f32_16x16x32_bf16 v[0:3], v[132:135], v[238:241], v[0:3]
	v_mfma_f32_16x16x32_bf16 v[4:7], v[140:143], v[238:241], v[4:7]
	s_setprio 0
	s_setprio 1
	v_mfma_f32_16x16x32_bf16 v[108:111], v[174:177], v[208:211], v[108:111]
	v_mfma_f32_16x16x32_bf16 v[116:119], v[182:185], v[208:211], v[116:119]
	v_mfma_f32_16x16x32_bf16 v[88:91], v[174:177], v[216:219], v[88:91]
	v_mfma_f32_16x16x32_bf16 v[100:103], v[182:185], v[216:219], v[100:103]
	v_mfma_f32_16x16x32_bf16 v[60:63], v[174:177], v[224:227], v[60:63]
	v_mfma_f32_16x16x32_bf16 v[76:79], v[182:185], v[224:227], v[76:79]
	v_mfma_f32_16x16x32_bf16 v[24:27], v[174:177], v[232:235], v[24:27]
	v_mfma_f32_16x16x32_bf16 v[44:47], v[182:185], v[232:235], v[44:47]
	v_mfma_f32_16x16x32_bf16 v[108:111], v[178:181], v[212:215], v[108:111]
	v_mfma_f32_16x16x32_bf16 v[116:119], v[186:189], v[212:215], v[116:119]
	v_mfma_f32_16x16x32_bf16 v[88:91], v[178:181], v[220:223], v[88:91]
	v_mfma_f32_16x16x32_bf16 v[100:103], v[186:189], v[220:223], v[100:103]
	v_mfma_f32_16x16x32_bf16 v[60:63], v[178:181], v[228:231], v[60:63]
	v_mfma_f32_16x16x32_bf16 v[76:79], v[186:189], v[228:231], v[76:79]
	v_mfma_f32_16x16x32_bf16 v[24:27], v[178:181], v[238:241], v[24:27]
	v_mfma_f32_16x16x32_bf16 v[44:47], v[186:189], v[238:241], v[44:47]
	s_setprio 0
	s_barrier
	s_add_i32 s81, s81, 2
	s_add_u32 s14, s14, 0x100
	s_addc_u32 s15, s15, 0
	s_add_u32 s79, s79, 0x100
	s_addc_u32 s80, s80, 0
	s_cmp_gt_u32 s81, 29

; __host__ __device__ __forceinline__ int perm_a64(int r) { return (r & ~63) + 4 * (r & 15) + ((r >> 4) & 3); }
; #define PG8_STAGE(bufoff, gbase, o0, o1) do { \
;         __builtin_amdgcn_global_load_lds((const unsigned*)((const char*)(gbase) + (o0)), (LAS unsigned*)(lds + (bufoff) + ldsw), 16, 0, 0); \
;         __builtin_amdgcn_global_load_lds((const unsigned*)((const char*)(gbase) + (o1)), (LAS unsigned*)(lds + (bufoff) + ldsw + 8192), 16, 0, 0); } while (0)
; #define PG8_WAIT_V(n) asm volatile("s_waitcnt vmcnt(" #n ")" ::: "memory")
; #define PG8_BAR __builtin_amdgcn_s_barrier()
; #define PG8_ACC_INIT(unit) do { if constexpr (Epi::ACC_INIT) { E.init(acc, unit, wr, wc, fr, fq); } else { \
;         _Pragma("unroll") for (int a = 0; a < 2; ++a) _Pragma("unroll") for (int b = 0; b < 2; ++b) _Pragma("unroll") for (int m = 0; m < 4; ++m) _Pragma("unroll") for (int n = 0; n < 2; ++n) acc[a][b][m][n] = (f32x4){0.f, 0.f, 0.f, 0.f}; } } while (0)
; template <class Epi, class Sched, class Prob>
; __device__ __forceinline__ void gemm_phase(LAS unsigned char* lds, LAS unsigned char* lds_epi, const Prob g, const Sched& S, const Epi& E, int wid) {
;     ...
;     Unit cur, nxt; int ui = 0; int epi_pm = -1;
;     if (!S.next(0, cur)) return;
;     const int Ra0 = aperm_of<Epi>::v ? perm_a64(R0) : R0, Ra1 = aperm_of<Epi>::v ? perm_a64(R1) : R1;
;     const unsigned cA00 = (unsigned)Ra0 * lda2 + (unsigned)C0 * 2u, cA01 = (unsigned)Ra1 * lda2 + (unsigned)C1 * 2u, cA10 = cA00 + (unsigned)HALF * lda2, cA11 = cA01 + (unsigned)HALF * lda2;
;     f32x4 acc[2][2][4][2];
;     ...
;     PG8_ACC_INIT(cur);
;     bf16x8 At[4][2], B0[2][2], B1[2][2];
;     const char* cA = g.a_base(cur); const char* cB = g.b_base(cur);
;     PG8_STAGE(PG8_SB(0, 0), cB, vB0, vB1); PG8_STAGE(PG8_SB(0, 1), cB + hstepB, vB0, vB1); PG8_STAGE(PG8_SA(0, 0), cA, cA00, cA01); PG8_STAGE(PG8_SA(0, 1), cA, cA10, cA11);
;     if (wr == 1) PG8_BAR;
;     PG8_WAIT_V(2); PG8_BAR;
;     PG8_STAGE(PG8_SB(1, 0), cB + kstep, vB0, vB1); PG8_STAGE(PG8_SA(1, 0), cA + kstep, cA00, cA01); PG8_STAGE(PG8_SB(1, 1), cB + hstepB + kstep, vB0, vB1);
;     PG8_WAIT_V(6); PG8_BAR;
.LBB0_1241:
	v_readlane_b32 s8, v254, 24
	s_lshr_b32 s3, s38, 3
	s_lshl_b32 s18, s8, 13
	s_add_u32 s12, s16, 0x41000000
	s_mov_b64 s[14:15], 0x80
	s_addc_u32 s13, s17, 0
	v_lshl_add_u64 v[4:5], v[4:5], 0, s[14:15]
	s_add_i32 m0, s29, 0x18000
	s_waitcnt vmcnt(2)
	s_barrier
	global_load_lds_dwordx4 v[4:5], off
	v_lshl_add_u64 v[2:3], v[2:3], 0, s[14:15]
	s_add_i32 m0, s29, 0x1a000
	s_add_i32 s48, s29, 0x8000
	s_add_i32 s49, s29, 0xa000
	global_load_lds_dwordx4 v[2:3], off
	v_lshl_add_u64 v[0:1], v[0:1], 0, s[14:15]
	s_mov_b32 m0, s48
	s_add_u32 s8, s30, 0x40080
	global_load_lds_dwordx4 v[0:1], off
	v_lshl_add_u64 v[0:1], v[6:7], 0, s[14:15]
	s_mov_b32 m0, s49
	s_addc_u32 s9, s31, 0
	global_load_lds_dwordx4 v[0:1], off
	v_lshl_add_u64 v[0:1], s[8:9], 0, v[162:163]
	s_add_i32 m0, s29, 0x1c000
	v_ashrrev_i32_e32 v2, 6, v10
	global_load_lds_dwordx4 v[0:1], off
	v_lshl_add_u64 v[0:1], s[8:9], 0, v[160:161]
	s_add_i32 m0, s29, 0x1e000
	v_readlane_b32 s8, v254, 16
	global_load_lds_dwordx4 v[0:1], off
	v_and_b32_e32 v1, 15, v10
	v_or_b32_e32 v190, s8, v1
	v_lshlrev_b32_e32 v3, 6, v190
	v_and_b32_e32 v4, 48, v10
	s_movk_i32 s8, 0x3c0
	v_lshlrev_b32_e32 v6, 2, v190
	v_and_or_b32 v3, v3, s8, v4
	v_lshl_add_u32 v5, v2, 10, s18
	v_and_b32_e32 v6, 32, v6
	v_bitop3_b32 v5, v3, v5, v6 bitop3:0xde
	v_lshl_or_b32 v3, v1, 6, v4
	v_lshlrev_b32_e32 v4, 2, v1
	v_ashrrev_i32_e32 v0, 1, v10
	v_add_lshl_u32 v2, v2, s3, 10
	v_and_b32_e32 v1, 32, v4
	v_and_b32_e32 v0, -8, v0
	v_bitop3_b32 v191, v3, v2, v1 bitop3:0xde
	v_add_u32_e32 v2, s91, v10
	v_ashrrev_i32_e32 v3, 31, v2
	v_ashrrev_i32_e32 v1, 31, v0
	v_lshl_add_u64 v[172:173], v[0:1], 0, s[38:39]
	v_lshl_add_u64 v[0:1], v[2:3], 2, s[16:17]
	s_mov_b64 s[16:17], 0x110000
	v_lshl_add_u64 v[174:175], v[0:1], 0, s[16:17]
	v_lshlrev_b32_e32 v0, 14, v8
	v_and_b32_e32 v0, 0xffff8000, v0
	v_lshl_add_u32 v0, v9, 11, v0
	v_and_b32_e32 v1, 1, v8
	v_lshl_or_b32 v0, v1, 6, v0
	v_lshlrev_b32_e32 v1, 1, v12
	v_add3_u32 v176, v0, v1, s47
	v_lshlrev_b32_e32 v0, 14, v11
	v_and_b32_e32 v0, 0xffff8000, v0
	s_waitcnt vmcnt(0)
	s_movk_i32 s3, 0x100
	v_lshl_add_u32 v0, v13, 11, v0
	v_and_b32_e32 v1, 1, v11
	v_cmp_gt_i32_e64 s[8:9], s3, v2
	s_add_i32 s3, 0, 0x20000
	v_lshl_or_b32 v0, v1, 6, v0
	v_lshlrev_b32_e32 v1, 1, v14
	s_add_i32 s50, 0, 0x10000
	s_add_i32 s51, 0, 0x14000
	v_mov_b32_e32 v167, v163
	v_mov_b32_e32 v171, v163
	v_lshl_add_u32 v192, v2, 2, s3
	v_add_u32_e32 v193, s74, v4
	v_mov_b32_e32 v177, v163
	v_add3_u32 v178, v0, v1, s47
	v_mov_b32_e32 v179, v163
	v_add_u32_e32 v194, s50, v191
	v_add_u32_e32 v195, s51, v191
	v_add_u32_e32 v196, 0, v5
	v_mov_b32_e32 v197, 0x358637bd
	v_mov_b32_e32 v198, 0x260
	s_mov_b64 s[16:17], 0x1c000
	s_mov_b64 s[18:19], 0x8c000
	v_mov_b64_e32 v[180:181], 0xdff
	s_barrier
	s_branch .LBB0_1244

; #define PG8_STAGE(bufoff, gbase, o0, o1) do { \
;         __builtin_amdgcn_global_load_lds((const unsigned*)((const char*)(gbase) + (o0)), (LAS unsigned*)(lds + (bufoff) + ldsw), 16, 0, 0); \
;         __builtin_amdgcn_global_load_lds((const unsigned*)((const char*)(gbase) + (o1)), (LAS unsigned*)(lds + (bufoff) + ldsw + 8192), 16, 0, 0); } while (0)
; #define PG8_LDA(dst, b, h) do { _Pragma("unroll") for (int m = 0; m < 4; ++m) _Pragma("unroll") for (int k = 0; k < 2; ++k) dst[m][k] = *(const LAS bf16x8*)(lds + PG8_SA(b, h) + aoff + m * 2048 + k * 1024); } while (0)
; #define PG8_LDB(dst, b, h) do { _Pragma("unroll") for (int n = 0; n < 2; ++n) _Pragma("unroll") for (int k = 0; k < 2; ++k) dst[n][k] = *(const LAS bf16x8*)(lds + PG8_SB(b, h) + boff + n * 2048 + k * 1024); } while (0)
; #define PG8_WAIT_V(n) asm volatile("s_waitcnt vmcnt(" #n ")" ::: "memory")
; #define PG8_WAIT_L(n) asm volatile("s_waitcnt lgkmcnt(" #n ")" ::: "memory")
; #define PG8_BAR __builtin_amdgcn_s_barrier()
; #define PG8_SCHED __builtin_amdgcn_sched_barrier(0)
; template <class Epi, class Sched, class Prob>
; __device__ __forceinline__ void gemm_phase(LAS unsigned char* lds, LAS unsigned char* lds_epi, const Prob g, const Sched& S, const Epi& E, int wid) {
;     ...
;         for (int t = 0; t < nt; t += 2) {
;             const bool last = (t == nt - 2);
;             const char* a1 = cA + (size_t)(t + 1) * kstep;
;             const char* a2 = last ? nA : cA + (size_t)(t + 2) * kstep; const char* b2 = last ? nB : cB + (size_t)(t + 2) * kstep;
;             const char* a3 = a2 + kstep; const char* b3 = b2 + kstep;
;             PG8_LDB(B0, 0, 0); PG8_LDB(B1, 0, 1); PG8_SCHED; PG8_LDA(At, 0, 0); PG8_STAGE(PG8_SA(1, 1), a1, cA10, cA11);
;             PG8_WAIT_V(8); PG8_WAIT_L(0); PG8_BAR; PG8_MMA(0, 0, At, B0); PG8_MMA(0, 1, At, B1); PG8_BAR; PG8_SCHED;
;             PG8_LDA(At, 0, 1); PG8_STAGE(PG8_SB(0, 0), b2, vB0, vB1); PG8_STAGE(PG8_SB(0, 1), b2 + hstepB, vB0, vB1); PG8_STAGE(PG8_SA(0, 0), a2, cA00, cA01);
;             PG8_WAIT_V(8); PG8_WAIT_L(0); PG8_BAR; PG8_MMA(1, 0, At, B0); PG8_MMA(1, 1, At, B1); PG8_BAR; PG8_SCHED;
.LBB0_1247:
	s_ashr_i32 s3, s2, 31
	s_lshl_b64 s[24:25], s[2:3], 19
	s_add_u32 s24, s36, s24
	s_addc_u32 s25, s37, s25
	s_and_b64 s[26:27], s[22:23], exec
	s_cselect_b32 s3, s25, s11
	s_cselect_b32 s54, s24, s10
	s_ashr_i32 s21, s20, 31
	s_lshl_b64 s[26:27], s[20:21], 19
	s_add_u32 s26, s40, s26
	s_addc_u32 s27, s41, s27
	s_and_b64 s[34:35], s[22:23], exec
	s_cselect_b32 s21, s27, s31
	s_cselect_b32 s55, s26, s30
	s_add_u32 s10, s10, 0x80
	s_addc_u32 s11, s11, 0
	s_add_u32 s56, s30, 0x100
	v_mov_b32_e32 v32, 0
	s_addc_u32 s58, s31, 0
	s_mov_b32 s59, -2
	ds_read_b128 v[24:27], v194
	ds_read_b128 v[28:31], v194 offset:1024
	ds_read_b128 v[16:19], v194 offset:2048
	ds_read_b128 v[20:23], v194 offset:3072
	ds_read_b128 v[8:11], v195
	ds_read_b128 v[12:15], v195 offset:1024
	ds_read_b128 v[0:3], v195 offset:2048
	ds_read_b128 v[4:7], v195 offset:3072
	s_add_u32 s30, s10, 0x80
	s_addc_u32 s31, s11, 0
	s_cmp_eq_u32 s59, 12
	s_cselect_b32 s35, s3, s31
	s_cselect_b32 s34, s54, s30
	s_cselect_b32 s31, s21, s58
	s_cselect_b32 s30, s55, s56
	v_lshl_add_u64 v[224:225], s[10:11], 0, v[178:179]
	s_add_i32 m0, s29, 0xc000
	ds_read_b128 v[182:185], v196
	ds_read_b128 v[186:189], v196 offset:1024
	ds_read_b128 v[200:203], v196 offset:2048
	ds_read_b128 v[204:207], v196 offset:3072
	ds_read_b128 v[208:211], v196 offset:4096
	ds_read_b128 v[212:215], v196 offset:5120
	ds_read_b128 v[216:219], v196 offset:6144
	ds_read_b128 v[220:223], v196 offset:7168
	global_load_lds_dwordx4 v[224:225], off
	v_lshl_add_u64 v[224:225], s[10:11], 0, v[176:177]
	s_add_i32 m0, s29, 0xe000
	s_nop 0
	global_load_lds_dwordx4 v[224:225], off
	s_waitcnt vmcnt(16)
	s_waitcnt lgkmcnt(0)
	s_barrier
	s_setprio 1
	s_waitcnt lgkmcnt(0)
	v_mfma_f32_16x16x128_f8f6f4 v[156:159], v[24:31], v[182:189], 0
	v_mfma_f32_16x16x128_f8f6f4 v[144:147], v[16:23], v[182:189], 0
	v_mfma_f32_16x16x128_f8f6f4 v[140:143], v[24:31], v[200:207], 0
	v_mfma_f32_16x16x128_f8f6f4 v[132:135], v[16:23], v[200:207], 0
	v_mfma_f32_16x16x128_f8f6f4 v[124:127], v[24:31], v[208:215], 0
	v_mfma_f32_16x16x128_f8f6f4 v[116:119], v[16:23], v[208:215], 0
	v_mfma_f32_16x16x128_f8f6f4 v[108:111], v[24:31], v[216:223], 0
	v_mfma_f32_16x16x128_f8f6f4 v[100:103], v[16:23], v[216:223], 0
	s_setprio 0
	s_setprio 1
	v_mfma_f32_16x16x128_f8f6f4 v[152:155], v[8:15], v[182:189], 0
	v_mfma_f32_16x16x128_f8f6f4 v[148:151], v[0:7], v[182:189], 0
	v_mfma_f32_16x16x128_f8f6f4 v[136:139], v[8:15], v[200:207], 0
	v_mfma_f32_16x16x128_f8f6f4 v[128:131], v[0:7], v[200:207], 0
	v_mfma_f32_16x16x128_f8f6f4 v[120:123], v[8:15], v[208:215], 0
	v_mfma_f32_16x16x128_f8f6f4 v[112:115], v[0:7], v[208:215], 0
	v_mfma_f32_16x16x128_f8f6f4 v[104:107], v[8:15], v[216:223], 0
	v_mfma_f32_16x16x128_f8f6f4 v[96:99], v[0:7], v[216:223], 0
	s_setprio 0
	s_barrier
	s_add_i32 s60, s50, s97
	v_lshl_add_u64 v[182:183], s[30:31], 0, v[162:163]
	s_mov_b32 m0, s60
	ds_read_b128 v[200:203], v196 offset:16384
	ds_read_b128 v[204:207], v196 offset:17408
	ds_read_b128 v[208:211], v196 offset:18432
	ds_read_b128 v[212:215], v196 offset:19456
	ds_read_b128 v[216:219], v196 offset:20480
	ds_read_b128 v[220:223], v196 offset:21504
	ds_read_b128 v[224:227], v196 offset:22528
	ds_read_b128 v[228:231], v196 offset:23552
	global_load_lds_dwordx4 v[182:183], off
	s_add_i32 m0, s60, 0x2000
	s_add_u32 s60, s30, 0x40000
	v_lshl_add_u64 v[184:185], s[30:31], 0, v[160:161]
	s_addc_u32 s61, s31, 0
	s_add_i32 s62, s51, s97
	global_load_lds_dwordx4 v[184:185], off
	v_lshl_add_u64 v[186:187], s[60:61], 0, v[162:163]
	s_mov_b32 m0, s62
	v_lshl_add_u64 v[188:189], s[34:35], 0, v[168:169]
	global_load_lds_dwordx4 v[186:187], off
	v_lshl_add_u64 v[186:187], s[60:61], 0, v[160:161]
	s_add_i32 m0, s62, 0x2000
	s_nop 0
	global_load_lds_dwordx4 v[186:187], off
	v_lshl_add_u64 v[186:187], s[34:35], 0, v[164:165]
	s_mov_b32 m0, s29
	s_nop 0
	global_load_lds_dwordx4 v[186:187], off
	s_mov_b32 m0, s43
	s_nop 0
	global_load_lds_dwordx4 v[188:189], off
	s_waitcnt vmcnt(16)
	s_waitcnt lgkmcnt(0)
	s_barrier
	s_setprio 1
	s_waitcnt lgkmcnt(0)
	v_mfma_f32_16x16x128_f8f6f4 v[92:95], v[24:31], v[200:207], 0
	v_mfma_f32_16x16x128_f8f6f4 v[84:87], v[16:23], v[200:207], 0
	v_mfma_f32_16x16x128_f8f6f4 v[76:79], v[24:31], v[208:215], 0
	v_mfma_f32_16x16x128_f8f6f4 v[68:71], v[16:23], v[208:215], 0
	v_mfma_f32_16x16x128_f8f6f4 v[60:63], v[24:31], v[216:223], 0
	v_mfma_f32_16x16x128_f8f6f4 v[52:55], v[16:23], v[216:223], 0
	v_mfma_f32_16x16x128_f8f6f4 v[44:47], v[24:31], v[224:231], 0
	v_mfma_f32_16x16x128_f8f6f4 v[36:39], v[16:23], v[224:231], 0
	s_setprio 0
	s_setprio 1
	v_mfma_f32_16x16x128_f8f6f4 v[88:91], v[8:15], v[200:207], 0
	v_mfma_f32_16x16x128_f8f6f4 v[80:83], v[0:7], v[200:207], 0
	v_mfma_f32_16x16x128_f8f6f4 v[72:75], v[8:15], v[208:215], 0
	v_mfma_f32_16x16x128_f8f6f4 v[64:67], v[0:7], v[208:215], 0
	v_mfma_f32_16x16x128_f8f6f4 v[56:59], v[8:15], v[216:223], 0
	v_mfma_f32_16x16x128_f8f6f4 v[48:51], v[0:7], v[216:223], 0
	v_mfma_f32_16x16x128_f8f6f4 v[40:43], v[8:15], v[224:231], 0
	v_mfma_f32_16x16x128_f8f6f4 v[32:35], v[0:7], v[224:231], 0
	s_setprio 0
	s_barrier
; #define PG8_STAGE(bufoff, gbase, o0, o1) do { \
;         __builtin_amdgcn_global_load_lds((const unsigned*)((const char*)(gbase) + (o0)), (LAS unsigned*)(lds + (bufoff) + ldsw), 16, 0, 0); \
;         __builtin_amdgcn_global_load_lds((const unsigned*)((const char*)(gbase) + (o1)), (LAS unsigned*)(lds + (bufoff) + ldsw + 8192), 16, 0, 0); } while (0)
; #define PG8_LDA(dst, b, h) do { _Pragma("unroll") for (int m = 0; m < 4; ++m) _Pragma("unroll") for (int k = 0; k < 2; ++k) dst[m][k] = *(const LAS bf16x8*)(lds + PG8_SA(b, h) + aoff + m * 2048 + k * 1024); } while (0)
; #define PG8_LDB(dst, b, h) do { _Pragma("unroll") for (int n = 0; n < 2; ++n) _Pragma("unroll") for (int k = 0; k < 2; ++k) dst[n][k] = *(const LAS bf16x8*)(lds + PG8_SB(b, h) + boff + n * 2048 + k * 1024); } while (0)
; #define PG8_WAIT_V(n) asm volatile("s_waitcnt vmcnt(" #n ")" ::: "memory")
; #define PG8_WAIT_L(n) asm volatile("s_waitcnt lgkmcnt(" #n ")" ::: "memory")
; #define PG8_BAR __builtin_amdgcn_s_barrier()
; #define PG8_SCHED __builtin_amdgcn_sched_barrier(0)
; template <class Epi, class Sched, class Prob>
; __device__ __forceinline__ void gemm_phase(LAS unsigned char* lds, LAS unsigned char* lds_epi, const Prob g, const Sched& S, const Epi& E, int wid) {
;     ...
;             PG8_LDB(B0, 1, 0); PG8_LDB(B1, 1, 1); PG8_SCHED; PG8_LDA(At, 1, 0); PG8_STAGE(PG8_SA(0, 1), a2, cA10, cA11);
;             PG8_WAIT_V(8); PG8_WAIT_L(0); PG8_BAR; PG8_MMA(0, 0, At, B0); PG8_MMA(0, 1, At, B1); PG8_BAR; PG8_SCHED;
;             PG8_LDA(At, 1, 1); PG8_STAGE(PG8_SB(1, 0), b3, vB0, vB1); PG8_STAGE(PG8_SB(1, 1), b3 + hstepB, vB0, vB1); PG8_STAGE(PG8_SA(1, 0), a3, cA00, cA01);
;             PG8_WAIT_V(8); PG8_WAIT_L(0); PG8_BAR; PG8_MMA(1, 0, At, B0); PG8_MMA(1, 1, At, B1); PG8_BAR; PG8_SCHED;
;         }
	s_add_i32 s60, 0, 0x18000
	s_add_i32 s61, 0, 0x1c000
	v_add_u32_e32 v12, s60, v191
	v_add_u32_e32 v28, s61, v191
	ds_read_b128 v[0:3], v12
	ds_read_b128 v[4:7], v12 offset:1024
	ds_read_b128 v[8:11], v12 offset:2048
	ds_read_b128 v[12:15], v12 offset:3072
	ds_read_b128 v[16:19], v28
	ds_read_b128 v[20:23], v28 offset:1024
	ds_read_b128 v[24:27], v28 offset:2048
	ds_read_b128 v[28:31], v28 offset:3072
	s_mov_b32 m0, s44
	v_lshl_add_u64 v[232:233], s[34:35], 0, v[166:167]
	ds_read_b128 v[200:203], v196 offset:32768
	ds_read_b128 v[204:207], v196 offset:33792
	ds_read_b128 v[208:211], v196 offset:34816
	ds_read_b128 v[212:215], v196 offset:35840
	ds_read_b128 v[216:219], v196 offset:36864
	ds_read_b128 v[220:223], v196 offset:37888
	ds_read_b128 v[224:227], v196 offset:38912
	ds_read_b128 v[228:231], v196 offset:39936
	global_load_lds_dwordx4 v[232:233], off
	v_lshl_add_u64 v[232:233], s[34:35], 0, v[170:171]
	s_mov_b32 m0, s45
	s_nop 0
	global_load_lds_dwordx4 v[232:233], off
	s_waitcnt vmcnt(8)
	s_waitcnt lgkmcnt(0)
	s_barrier
	s_setprio 1
	s_waitcnt lgkmcnt(0)
	v_mfma_f32_16x16x128_f8f6f4 v[156:159], v[0:7], v[200:207], v[156:159]
	v_mfma_f32_16x16x128_f8f6f4 v[144:147], v[8:15], v[200:207], v[144:147]
	v_mfma_f32_16x16x128_f8f6f4 v[140:143], v[0:7], v[208:215], v[140:143]
	v_mfma_f32_16x16x128_f8f6f4 v[132:135], v[8:15], v[208:215], v[132:135]
	v_mfma_f32_16x16x128_f8f6f4 v[124:127], v[0:7], v[216:223], v[124:127]
	v_mfma_f32_16x16x128_f8f6f4 v[116:119], v[8:15], v[216:223], v[116:119]
	v_mfma_f32_16x16x128_f8f6f4 v[108:111], v[0:7], v[224:231], v[108:111]
	v_mfma_f32_16x16x128_f8f6f4 v[100:103], v[8:15], v[224:231], v[100:103]
	s_setprio 0
	s_setprio 1
	v_mfma_f32_16x16x128_f8f6f4 v[152:155], v[16:23], v[200:207], v[152:155]
	v_mfma_f32_16x16x128_f8f6f4 v[148:151], v[24:31], v[200:207], v[148:151]
	v_mfma_f32_16x16x128_f8f6f4 v[136:139], v[16:23], v[208:215], v[136:139]
	v_mfma_f32_16x16x128_f8f6f4 v[128:131], v[24:31], v[208:215], v[128:131]
	v_mfma_f32_16x16x128_f8f6f4 v[120:123], v[16:23], v[216:223], v[120:123]
	v_mfma_f32_16x16x128_f8f6f4 v[112:115], v[24:31], v[216:223], v[112:115]
	v_mfma_f32_16x16x128_f8f6f4 v[104:107], v[16:23], v[224:231], v[104:107]
	v_mfma_f32_16x16x128_f8f6f4 v[96:99], v[24:31], v[224:231], v[96:99]
	s_setprio 0
	s_barrier
	s_add_i32 s34, s60, s97
	v_lshl_add_u64 v[182:183], v[182:183], 0, s[14:15]
	s_mov_b32 m0, s34
	ds_read_b128 v[200:203], v196 offset:49152
	ds_read_b128 v[204:207], v196 offset:50176
	ds_read_b128 v[208:211], v196 offset:51200
	ds_read_b128 v[212:215], v196 offset:52224
	ds_read_b128 v[216:219], v196 offset:53248
	ds_read_b128 v[220:223], v196 offset:54272
	ds_read_b128 v[224:227], v196 offset:55296
	ds_read_b128 v[228:231], v196 offset:56320
	global_load_lds_dwordx4 v[182:183], off
	s_add_i32 m0, s34, 0x2000
	s_add_u32 s30, s30, 0x40080
	v_lshl_add_u64 v[182:183], v[184:185], 0, s[14:15]
	s_addc_u32 s31, s31, 0
	s_add_i32 s34, s61, s97
	global_load_lds_dwordx4 v[182:183], off
	v_lshl_add_u64 v[182:183], s[30:31], 0, v[162:163]
	s_mov_b32 m0, s34
	s_nop 0
	global_load_lds_dwordx4 v[182:183], off
	v_lshl_add_u64 v[182:183], s[30:31], 0, v[160:161]
	s_add_i32 m0, s34, 0x2000
	s_nop 0
	global_load_lds_dwordx4 v[182:183], off
	v_lshl_add_u64 v[182:183], v[186:187], 0, s[14:15]
	s_mov_b32 m0, s48
	s_nop 0
	global_load_lds_dwordx4 v[182:183], off
	v_lshl_add_u64 v[182:183], v[188:189], 0, s[14:15]
	s_mov_b32 m0, s49
	s_nop 0
	global_load_lds_dwordx4 v[182:183], off
	s_waitcnt vmcnt(8)
	s_waitcnt lgkmcnt(0)
	s_barrier
	s_setprio 1
	s_waitcnt lgkmcnt(0)
	v_mfma_f32_16x16x128_f8f6f4 v[92:95], v[0:7], v[200:207], v[92:95]
	v_mfma_f32_16x16x128_f8f6f4 v[84:87], v[8:15], v[200:207], v[84:87]
	v_mfma_f32_16x16x128_f8f6f4 v[76:79], v[0:7], v[208:215], v[76:79]
	v_mfma_f32_16x16x128_f8f6f4 v[68:71], v[8:15], v[208:215], v[68:71]
	v_mfma_f32_16x16x128_f8f6f4 v[60:63], v[0:7], v[216:223], v[60:63]
	v_mfma_f32_16x16x128_f8f6f4 v[52:55], v[8:15], v[216:223], v[52:55]
	v_mfma_f32_16x16x128_f8f6f4 v[44:47], v[0:7], v[224:231], v[44:47]
	v_mfma_f32_16x16x128_f8f6f4 v[36:39], v[8:15], v[224:231], v[36:39]
	s_setprio 0
	s_setprio 1
	v_mfma_f32_16x16x128_f8f6f4 v[88:91], v[16:23], v[200:207], v[88:91]
	v_mfma_f32_16x16x128_f8f6f4 v[80:83], v[24:31], v[200:207], v[80:83]
	v_mfma_f32_16x16x128_f8f6f4 v[72:75], v[16:23], v[208:215], v[72:75]
	v_mfma_f32_16x16x128_f8f6f4 v[64:67], v[24:31], v[208:215], v[64:67]
	v_mfma_f32_16x16x128_f8f6f4 v[56:59], v[16:23], v[216:223], v[56:59]
	v_mfma_f32_16x16x128_f8f6f4 v[48:51], v[24:31], v[216:223], v[48:51]
	v_mfma_f32_16x16x128_f8f6f4 v[40:43], v[16:23], v[224:231], v[40:43]
	v_mfma_f32_16x16x128_f8f6f4 v[32:35], v[24:31], v[224:231], v[32:35]
	s_setprio 0
	s_barrier
	s_add_i32 s59, s59, 2
	s_add_u32 s10, s10, 0x100
	s_addc_u32 s11, s11, 0
	s_add_u32 s56, s56, 0x100
	s_addc_u32 s58, s58, 0
	s_cmp_gt_u32 s59, 13

; __host__ __device__ __forceinline__ int perm_a64(int r) { return (r & ~63) + 4 * (r & 15) + ((r >> 4) & 3); }
; #define PG8_STAGE(bufoff, gbase, o0, o1) do { \
;         __builtin_amdgcn_global_load_lds((const unsigned*)((const char*)(gbase) + (o0)), (LAS unsigned*)(lds + (bufoff) + ldsw), 16, 0, 0); \
;         __builtin_amdgcn_global_load_lds((const unsigned*)((const char*)(gbase) + (o1)), (LAS unsigned*)(lds + (bufoff) + ldsw + 8192), 16, 0, 0); } while (0)
; #define PG8_WAIT_V(n) asm volatile("s_waitcnt vmcnt(" #n ")" ::: "memory")
; #define PG8_BAR __builtin_amdgcn_s_barrier()
; #define PG8_ACC_INIT(unit) do { if constexpr (Epi::ACC_INIT) { E.init(acc, unit, wr, wc, fr, fq); } else { \
;         _Pragma("unroll") for (int a = 0; a < 2; ++a) _Pragma("unroll") for (int b = 0; b < 2; ++b) _Pragma("unroll") for (int m = 0; m < 4; ++m) _Pragma("unroll") for (int n = 0; n < 2; ++n) acc[a][b][m][n] = (f32x4){0.f, 0.f, 0.f, 0.f}; } } while (0)
; template <class Epi, class Sched, class Prob>
; __device__ __forceinline__ void gemm_phase(LAS unsigned char* lds, LAS unsigned char* lds_epi, const Prob g, const Sched& S, const Epi& E, int wid) {
;     ...
;     Unit cur, nxt; int ui = 0; int epi_pm = -1;
;     if (!S.next(0, cur)) return;
;     const int Ra0 = aperm_of<Epi>::v ? perm_a64(R0) : R0, Ra1 = aperm_of<Epi>::v ? perm_a64(R1) : R1;
;     const unsigned cA00 = (unsigned)Ra0 * lda2 + (unsigned)C0 * 2u, cA01 = (unsigned)Ra1 * lda2 + (unsigned)C1 * 2u, cA10 = cA00 + (unsigned)HALF * lda2, cA11 = cA01 + (unsigned)HALF * lda2;
;     f32x4 acc[2][2][4][2];
;     ...
;     PG8_ACC_INIT(cur);
;     bf16x8 At[4][2], B0[2][2], B1[2][2];
;     const char* cA = g.a_base(cur); const char* cB = g.b_base(cur);
;     PG8_STAGE(PG8_SB(0, 0), cB, vB0, vB1); PG8_STAGE(PG8_SB(0, 1), cB + hstepB, vB0, vB1); PG8_STAGE(PG8_SA(0, 0), cA, cA00, cA01); PG8_STAGE(PG8_SA(0, 1), cA, cA10, cA11);
;     if (wr == 1) PG8_BAR;
;     PG8_WAIT_V(2); PG8_BAR;
;     PG8_STAGE(PG8_SB(1, 0), cB + kstep, vB0, vB1); PG8_STAGE(PG8_SA(1, 0), cA + kstep, cA00, cA01); PG8_STAGE(PG8_SB(1, 1), cB + hstepB + kstep, vB0, vB1);
;     PG8_WAIT_V(6); PG8_BAR;
.LBB0_1423:
	v_readlane_b32 s24, v254, 24
	s_lshr_b32 s17, s38, 3
	s_lshl_b32 s22, s24, 13
	s_add_u32 s18, s2, 0x49000000
	s_addc_u32 s19, s3, 0
	s_add_u32 s20, s2, 0x45000000
	s_addc_u32 s21, s3, 0
	s_add_u32 s69, s2, 0x190000
	v_and_b32_e32 v18, 15, v237
	v_readlane_b32 s23, v254, 16
	s_addc_u32 s70, s3, 0
	s_add_u32 s71, s2, 0x900000
	v_or_b32_e32 v19, s23, v18
	v_ashrrev_i32_e32 v20, 6, v237
	v_lshlrev_b32_e32 v21, 6, v19
	v_and_b32_e32 v22, 48, v237
	s_movk_i32 s23, 0x3c0
	s_addc_u32 s72, s3, 0
	v_and_or_b32 v21, v21, s23, v22
	v_lshl_add_u32 v23, v20, 10, s22
	v_readlane_b32 s22, v254, 4
	v_readlane_b32 s23, v254, 5
	s_add_u32 s73, s22, 0xd200
	v_add_lshl_u32 v20, v20, s17, 10
	s_addc_u32 s76, s23, 0
	v_readlane_b32 s17, v254, 31
	s_cmpk_gt_u32 s17, 0x2ff
	s_mul_i32 s17, s24, 0x600
	s_mov_b64 s[24:25], 0x80
	s_cselect_b64 s[22:23], -1, 0
	s_add_i32 s77, s17, 0
	v_lshl_add_u64 v[4:5], v[4:5], 0, s[24:25]
	s_add_i32 m0, s62, 0x18000
	s_add_i32 s77, s77, 0x20400
	s_waitcnt vmcnt(2)
	s_barrier
	global_load_lds_dwordx4 v[4:5], off
	v_lshl_add_u64 v[2:3], v[2:3], 0, s[24:25]
	s_add_i32 m0, s62, 0x1a000
	s_add_i32 s78, s62, 0x8000
	s_add_i32 s79, s62, 0xa000
	global_load_lds_dwordx4 v[2:3], off
	v_lshl_add_u64 v[0:1], v[0:1], 0, s[24:25]
	s_mov_b32 m0, s78
	s_add_u32 s26, s46, 0x80080
	global_load_lds_dwordx4 v[0:1], off
	v_lshl_add_u64 v[0:1], v[6:7], 0, s[24:25]
	s_mov_b32 m0, s79
	s_addc_u32 s27, s47, 0
	global_load_lds_dwordx4 v[0:1], off
	v_lshl_add_u64 v[0:1], s[26:27], 0, v[128:129]
	s_add_i32 m0, s62, 0x1c000
	v_lshlrev_b32_e32 v19, 2, v19
	global_load_lds_dwordx4 v[0:1], off
	v_lshl_add_u64 v[0:1], s[26:27], 0, v[130:131]
	s_add_i32 m0, s62, 0x1e000
	s_add_u32 s26, s12, 0x2000
	global_load_lds_dwordx4 v[0:1], off
	v_and_b32_e32 v1, 1, v10
	v_add3_u32 v0, v15, v16, v17
	v_lshlrev_b32_e32 v1, 6, v1
	v_lshl_or_b32 v0, v0, 12, v1
	v_lshlrev_b32_e32 v1, 1, v11
	s_addc_u32 s27, s13, 0
	v_add3_u32 v0, v0, v1, s68
	v_mov_b32_e32 v1, v129
	v_and_b32_e32 v19, 32, v19
	s_add_u32 s28, s12, 0x4000
	v_lshl_add_u64 v[140:141], v[0:1], 0, s[24:25]
	v_and_b32_e32 v1, 1, v8
	v_bitop3_b32 v19, v21, v23, v19 bitop3:0xde
	v_lshlrev_b32_e32 v21, 2, v237
	s_addc_u32 s29, s13, 0
	v_add3_u32 v0, v12, v13, v14
	v_lshlrev_b32_e32 v1, 6, v1
	v_lshl_or_b32 v18, v18, 6, v22
	v_and_b32_e32 v21, 32, v21
	s_waitcnt vmcnt(0)
	s_add_u32 s30, s12, 0x6000
	v_lshl_or_b32 v0, v0, 12, v1
	v_lshlrev_b32_e32 v1, 1, v9
	v_bitop3_b32 v239, v18, v20, v21 bitop3:0xde
	s_addc_u32 s31, s13, 0
	v_add3_u32 v0, v0, v1, s68
	v_mov_b32_e32 v1, v129
	s_add_i32 s80, 0, 0x10000
	s_add_i32 s81, 0, 0x14000
	v_mov_b32_e32 v135, v129
	v_mov_b32_e32 v139, v129
	v_lshl_add_u64 v[142:143], v[0:1], 0, s[24:25]
	v_add_u32_e32 v240, s80, v239
	v_add_u32_e32 v241, s81, v239
	v_add_u32_e32 v242, 0, v19
	v_mov_b32_e32 v243, 0x358637bd
	v_mov_b32_e32 v236, 0x260
	s_movk_i32 s82, 0x1000
	s_movk_i32 s83, 0x3000
	s_mov_b32 s84, 0x81000
	s_mov_b32 s85, 0x83000
	v_mov_b64_e32 v[144:145], 0x3ff
	s_barrier
	s_branch .LBB0_1426

; #define PG8_STAGE(bufoff, gbase, o0, o1) do { \
;         __builtin_amdgcn_global_load_lds((const unsigned*)((const char*)(gbase) + (o0)), (LAS unsigned*)(lds + (bufoff) + ldsw), 16, 0, 0); \
;         __builtin_amdgcn_global_load_lds((const unsigned*)((const char*)(gbase) + (o1)), (LAS unsigned*)(lds + (bufoff) + ldsw + 8192), 16, 0, 0); } while (0)
; #define PG8_LDA(dst, b, h) do { _Pragma("unroll") for (int m = 0; m < 4; ++m) _Pragma("unroll") for (int k = 0; k < 2; ++k) dst[m][k] = *(const LAS bf16x8*)(lds + PG8_SA(b, h) + aoff + m * 2048 + k * 1024); } while (0)
; #define PG8_LDB(dst, b, h) do { _Pragma("unroll") for (int n = 0; n < 2; ++n) _Pragma("unroll") for (int k = 0; k < 2; ++k) dst[n][k] = *(const LAS bf16x8*)(lds + PG8_SB(b, h) + boff + n * 2048 + k * 1024); } while (0)
; #define PG8_WAIT_V(n) asm volatile("s_waitcnt vmcnt(" #n ")" ::: "memory")
; #define PG8_WAIT_L(n) asm volatile("s_waitcnt lgkmcnt(" #n ")" ::: "memory")
; #define PG8_BAR __builtin_amdgcn_s_barrier()
; #define PG8_SCHED __builtin_amdgcn_sched_barrier(0)
; template <class Epi, class Sched, class Prob>
; __device__ __forceinline__ void gemm_phase(LAS unsigned char* lds, LAS unsigned char* lds_epi, const Prob g, const Sched& S, const Epi& E, int wid) {
;     ...
;         for (int t = 0; t < nt; t += 2) {
;             const bool last = (t == nt - 2);
;             const char* a1 = cA + (size_t)(t + 1) * kstep;
;             const char* a2 = last ? nA : cA + (size_t)(t + 2) * kstep; const char* b2 = last ? nB : cB + (size_t)(t + 2) * kstep;
;             const char* a3 = a2 + kstep; const char* b3 = b2 + kstep;
;             PG8_LDB(B0, 0, 0); PG8_LDB(B1, 0, 1); PG8_SCHED; PG8_LDA(At, 0, 0); PG8_STAGE(PG8_SA(1, 1), a1, cA10, cA11);
;             PG8_WAIT_V(8); PG8_WAIT_L(0); PG8_BAR; PG8_MMA(0, 0, At, B0); PG8_MMA(0, 1, At, B1); PG8_BAR; PG8_SCHED;
;             PG8_LDA(At, 0, 1); PG8_STAGE(PG8_SB(0, 0), b2, vB0, vB1); PG8_STAGE(PG8_SB(0, 1), b2 + hstepB, vB0, vB1); PG8_STAGE(PG8_SA(0, 0), a2, cA00, cA01);
;             PG8_WAIT_V(8); PG8_WAIT_L(0); PG8_BAR; PG8_MMA(1, 0, At, B0); PG8_MMA(1, 1, At, B1); PG8_BAR; PG8_SCHED;
.LBB0_1433:
	s_ashr_i32 s17, s16, 31
	s_lshl_b64 s[40:41], s[16:17], 20
	s_add_u32 s40, s58, s40
	s_addc_u32 s41, s59, s41
	s_and_b64 s[42:43], s[36:37], exec
	s_cselect_b32 s17, s41, s11
	s_cselect_b32 s52, s40, s10
	s_ashr_i32 s35, s34, 31
	s_lshl_b64 s[42:43], s[34:35], 20
	s_add_u32 s42, s60, s42
	s_addc_u32 s43, s61, s43
	s_and_b64 s[48:49], s[36:37], exec
	s_cselect_b32 s35, s43, s47
	s_cselect_b32 s53, s42, s46
	s_add_u32 s54, s46, 0x100
	v_mov_b32_e32 v0, 0
	s_addc_u32 s55, s47, 0
	s_mov_b32 s87, -2
	ds_read_b128 v[146:149], v240
	ds_read_b128 v[150:153], v240 offset:1024
	ds_read_b128 v[154:157], v240 offset:2048
	ds_read_b128 v[158:161], v240 offset:3072
	ds_read_b128 v[162:165], v241
	ds_read_b128 v[166:169], v241 offset:1024
	ds_read_b128 v[170:173], v241 offset:2048
	ds_read_b128 v[174:177], v241 offset:3072
	s_add_u32 s46, s10, 0x100
	s_addc_u32 s47, s11, 0
	s_cmp_eq_u32 s87, 28
	s_cselect_b32 s51, s17, s47
	s_cselect_b32 s50, s52, s46
	s_cselect_b32 s49, s35, s55
	s_cselect_b32 s48, s53, s54
	v_lshl_add_u64 v[210:211], s[10:11], 0, v[142:143]
	s_add_i32 m0, s62, 0xc000
	ds_read_b128 v[178:181], v242
	ds_read_b128 v[182:185], v242 offset:1024
	ds_read_b128 v[186:189], v242 offset:2048
	ds_read_b128 v[190:193], v242 offset:3072
	ds_read_b128 v[194:197], v242 offset:4096
	ds_read_b128 v[198:201], v242 offset:5120
	ds_read_b128 v[202:205], v242 offset:6144
	ds_read_b128 v[206:209], v242 offset:7168
	global_load_lds_dwordx4 v[210:211], off
	v_lshl_add_u64 v[210:211], s[10:11], 0, v[140:141]
	s_add_i32 m0, s62, 0xe000
	s_nop 0
	global_load_lds_dwordx4 v[210:211], off
	s_waitcnt vmcnt(22)
	s_waitcnt lgkmcnt(0)
	s_barrier
	s_setprio 1
	s_waitcnt lgkmcnt(0)
	v_mfma_f32_16x16x32_bf16 v[124:127], v[146:149], v[178:181], 0
	v_mfma_f32_16x16x32_bf16 v[120:123], v[154:157], v[178:181], 0
	v_mfma_f32_16x16x32_bf16 v[116:119], v[146:149], v[186:189], 0
	v_mfma_f32_16x16x32_bf16 v[112:115], v[154:157], v[186:189], 0
	v_mfma_f32_16x16x32_bf16 v[108:111], v[146:149], v[194:197], 0
	v_mfma_f32_16x16x32_bf16 v[100:103], v[154:157], v[194:197], 0
	v_mfma_f32_16x16x32_bf16 v[92:95], v[146:149], v[202:205], 0
	v_mfma_f32_16x16x32_bf16 v[84:87], v[154:157], v[202:205], 0
	v_mfma_f32_16x16x32_bf16 v[124:127], v[150:153], v[182:185], v[124:127]
	v_mfma_f32_16x16x32_bf16 v[120:123], v[158:161], v[182:185], v[120:123]
	v_mfma_f32_16x16x32_bf16 v[116:119], v[150:153], v[190:193], v[116:119]
	v_mfma_f32_16x16x32_bf16 v[112:115], v[158:161], v[190:193], v[112:115]
	v_mfma_f32_16x16x32_bf16 v[108:111], v[150:153], v[198:201], v[108:111]
	v_mfma_f32_16x16x32_bf16 v[100:103], v[158:161], v[198:201], v[100:103]
	v_mfma_f32_16x16x32_bf16 v[92:95], v[150:153], v[206:209], v[92:95]
	v_mfma_f32_16x16x32_bf16 v[84:87], v[158:161], v[206:209], v[84:87]
	s_setprio 0
	s_setprio 1
	v_mfma_f32_16x16x32_bf16 v[104:107], v[162:165], v[178:181], 0
	v_mfma_f32_16x16x32_bf16 v[96:99], v[170:173], v[178:181], 0
	v_mfma_f32_16x16x32_bf16 v[88:91], v[162:165], v[186:189], 0
	v_mfma_f32_16x16x32_bf16 v[80:83], v[170:173], v[186:189], 0
	v_mfma_f32_16x16x32_bf16 v[76:79], v[162:165], v[194:197], 0
	v_mfma_f32_16x16x32_bf16 v[72:75], v[170:173], v[194:197], 0
	v_mfma_f32_16x16x32_bf16 v[68:71], v[162:165], v[202:205], 0
	v_mfma_f32_16x16x32_bf16 v[64:67], v[170:173], v[202:205], 0
	v_mfma_f32_16x16x32_bf16 v[104:107], v[166:169], v[182:185], v[104:107]
	v_mfma_f32_16x16x32_bf16 v[96:99], v[174:177], v[182:185], v[96:99]
	v_mfma_f32_16x16x32_bf16 v[88:91], v[166:169], v[190:193], v[88:91]
	v_mfma_f32_16x16x32_bf16 v[80:83], v[174:177], v[190:193], v[80:83]
	v_mfma_f32_16x16x32_bf16 v[76:79], v[166:169], v[198:201], v[76:79]
	v_mfma_f32_16x16x32_bf16 v[72:75], v[174:177], v[198:201], v[72:75]
	v_mfma_f32_16x16x32_bf16 v[68:71], v[166:169], v[206:209], v[68:71]
	v_mfma_f32_16x16x32_bf16 v[64:67], v[174:177], v[206:209], v[64:67]
	s_setprio 0
	s_barrier
	s_add_i32 s10, s80, s97
	v_lshl_add_u64 v[210:211], s[48:49], 0, v[128:129]
	s_mov_b32 m0, s10
	ds_read_b128 v[178:181], v242 offset:16384
	ds_read_b128 v[182:185], v242 offset:17408
	ds_read_b128 v[186:189], v242 offset:18432
	ds_read_b128 v[190:193], v242 offset:19456
	ds_read_b128 v[194:197], v242 offset:20480
	ds_read_b128 v[198:201], v242 offset:21504
	ds_read_b128 v[202:205], v242 offset:22528
	ds_read_b128 v[206:209], v242 offset:23552
	global_load_lds_dwordx4 v[210:211], off
	s_add_i32 m0, s10, 0x2000
	s_add_u32 s10, s48, 0x80000
	v_lshl_add_u64 v[212:213], s[48:49], 0, v[130:131]
	s_addc_u32 s11, s49, 0
	s_add_i32 s88, s81, s97
	global_load_lds_dwordx4 v[212:213], off
	v_lshl_add_u64 v[214:215], s[10:11], 0, v[128:129]
	s_mov_b32 m0, s88
	v_lshl_add_u64 v[216:217], s[50:51], 0, v[136:137]
	global_load_lds_dwordx4 v[214:215], off
	v_lshl_add_u64 v[214:215], s[10:11], 0, v[130:131]
	s_add_i32 m0, s88, 0x2000
	s_nop 0
	global_load_lds_dwordx4 v[214:215], off
	v_lshl_add_u64 v[214:215], s[50:51], 0, v[132:133]
	s_mov_b32 m0, s62
	s_nop 0
	global_load_lds_dwordx4 v[214:215], off
	s_mov_b32 m0, s63
	s_nop 0
	global_load_lds_dwordx4 v[216:217], off
	s_waitcnt vmcnt(22)
	s_waitcnt lgkmcnt(0)
	s_barrier
; #define PG8_STAGE(bufoff, gbase, o0, o1) do { \
;         __builtin_amdgcn_global_load_lds((const unsigned*)((const char*)(gbase) + (o0)), (LAS unsigned*)(lds + (bufoff) + ldsw), 16, 0, 0); \
;         __builtin_amdgcn_global_load_lds((const unsigned*)((const char*)(gbase) + (o1)), (LAS unsigned*)(lds + (bufoff) + ldsw + 8192), 16, 0, 0); } while (0)
; #define PG8_LDA(dst, b, h) do { _Pragma("unroll") for (int m = 0; m < 4; ++m) _Pragma("unroll") for (int k = 0; k < 2; ++k) dst[m][k] = *(const LAS bf16x8*)(lds + PG8_SA(b, h) + aoff + m * 2048 + k * 1024); } while (0)
; #define PG8_LDB(dst, b, h) do { _Pragma("unroll") for (int n = 0; n < 2; ++n) _Pragma("unroll") for (int k = 0; k < 2; ++k) dst[n][k] = *(const LAS bf16x8*)(lds + PG8_SB(b, h) + boff + n * 2048 + k * 1024); } while (0)
; #define PG8_WAIT_V(n) asm volatile("s_waitcnt vmcnt(" #n ")" ::: "memory")
; #define PG8_WAIT_L(n) asm volatile("s_waitcnt lgkmcnt(" #n ")" ::: "memory")
; #define PG8_BAR __builtin_amdgcn_s_barrier()
; #define PG8_SCHED __builtin_amdgcn_sched_barrier(0)
; template <class Epi, class Sched, class Prob>
; __device__ __forceinline__ void gemm_phase(LAS unsigned char* lds, LAS unsigned char* lds_epi, const Prob g, const Sched& S, const Epi& E, int wid) {
;     ...
;             PG8_WAIT_V(8); PG8_WAIT_L(0); PG8_BAR; PG8_MMA(0, 0, At, B0); PG8_MMA(0, 1, At, B1); PG8_BAR; PG8_SCHED;
;             PG8_LDA(At, 0, 1); PG8_STAGE(PG8_SB(0, 0), b2, vB0, vB1); PG8_STAGE(PG8_SB(0, 1), b2 + hstepB, vB0, vB1); PG8_STAGE(PG8_SA(0, 0), a2, cA00, cA01);
;             PG8_WAIT_V(8); PG8_WAIT_L(0); PG8_BAR; PG8_MMA(1, 0, At, B0); PG8_MMA(1, 1, At, B1); PG8_BAR; PG8_SCHED;
;             PG8_LDB(B0, 1, 0); PG8_LDB(B1, 1, 1); PG8_SCHED; PG8_LDA(At, 1, 0); PG8_STAGE(PG8_SA(0, 1), a2, cA10, cA11);
;             PG8_WAIT_V(8); PG8_WAIT_L(0); PG8_BAR; PG8_MMA(0, 0, At, B0); PG8_MMA(0, 1, At, B1); PG8_BAR; PG8_SCHED;
;             PG8_LDA(At, 1, 1); PG8_STAGE(PG8_SB(1, 0), b3, vB0, vB1); PG8_STAGE(PG8_SB(1, 1), b3 + hstepB, vB0, vB1); PG8_STAGE(PG8_SA(1, 0), a3, cA00, cA01);
	s_setprio 1
	s_waitcnt lgkmcnt(0)
	v_mfma_f32_16x16x32_bf16 v[60:63], v[146:149], v[178:181], 0
	v_mfma_f32_16x16x32_bf16 v[56:59], v[154:157], v[178:181], 0
	v_mfma_f32_16x16x32_bf16 v[52:55], v[146:149], v[186:189], 0
	v_mfma_f32_16x16x32_bf16 v[48:51], v[154:157], v[186:189], 0
	v_mfma_f32_16x16x32_bf16 v[36:39], v[146:149], v[194:197], 0
	v_mfma_f32_16x16x32_bf16 v[32:35], v[154:157], v[194:197], 0
	v_mfma_f32_16x16x32_bf16 v[20:23], v[146:149], v[202:205], 0
	v_mfma_f32_16x16x32_bf16 v[16:19], v[154:157], v[202:205], 0
	v_mfma_f32_16x16x32_bf16 v[60:63], v[150:153], v[182:185], v[60:63]
	v_mfma_f32_16x16x32_bf16 v[56:59], v[158:161], v[182:185], v[56:59]
	v_mfma_f32_16x16x32_bf16 v[52:55], v[150:153], v[190:193], v[52:55]
	v_mfma_f32_16x16x32_bf16 v[48:51], v[158:161], v[190:193], v[48:51]
	v_mfma_f32_16x16x32_bf16 v[36:39], v[150:153], v[198:201], v[36:39]
	v_mfma_f32_16x16x32_bf16 v[32:35], v[158:161], v[198:201], v[32:35]
	v_mfma_f32_16x16x32_bf16 v[20:23], v[150:153], v[206:209], v[20:23]
	v_mfma_f32_16x16x32_bf16 v[16:19], v[158:161], v[206:209], v[16:19]
	s_setprio 0
	s_setprio 1
	v_mfma_f32_16x16x32_bf16 v[44:47], v[162:165], v[178:181], 0
	v_mfma_f32_16x16x32_bf16 v[40:43], v[170:173], v[178:181], 0
	v_mfma_f32_16x16x32_bf16 v[28:31], v[162:165], v[186:189], 0
	v_mfma_f32_16x16x32_bf16 v[24:27], v[170:173], v[186:189], 0
	v_mfma_f32_16x16x32_bf16 v[12:15], v[162:165], v[194:197], 0
	v_mfma_f32_16x16x32_bf16 v[8:11], v[170:173], v[194:197], 0
	v_mfma_f32_16x16x32_bf16 v[4:7], v[162:165], v[202:205], 0
	v_mfma_f32_16x16x32_bf16 v[0:3], v[170:173], v[202:205], 0
	v_mfma_f32_16x16x32_bf16 v[44:47], v[166:169], v[182:185], v[44:47]
	v_mfma_f32_16x16x32_bf16 v[40:43], v[174:177], v[182:185], v[40:43]
	v_mfma_f32_16x16x32_bf16 v[28:31], v[166:169], v[190:193], v[28:31]
	v_mfma_f32_16x16x32_bf16 v[24:27], v[174:177], v[190:193], v[24:27]
	v_mfma_f32_16x16x32_bf16 v[12:15], v[166:169], v[198:201], v[12:15]
	v_mfma_f32_16x16x32_bf16 v[8:11], v[174:177], v[198:201], v[8:11]
	v_mfma_f32_16x16x32_bf16 v[4:7], v[166:169], v[206:209], v[4:7]
	v_mfma_f32_16x16x32_bf16 v[0:3], v[174:177], v[206:209], v[0:3]
	s_setprio 0
	s_barrier
	s_add_i32 s10, 0, 0x18000
	s_add_i32 s88, 0, 0x1c000
	v_add_u32_e32 v158, s10, v239
	v_add_u32_e32 v174, s88, v239
	ds_read_b128 v[146:149], v158
	ds_read_b128 v[150:153], v158 offset:1024
	ds_read_b128 v[154:157], v158 offset:2048
	ds_read_b128 v[158:161], v158 offset:3072
	ds_read_b128 v[162:165], v174
	ds_read_b128 v[166:169], v174 offset:1024
	ds_read_b128 v[170:173], v174 offset:2048
	ds_read_b128 v[174:177], v174 offset:3072
	s_mov_b32 m0, s64
	v_lshl_add_u64 v[218:219], s[50:51], 0, v[134:135]
	ds_read_b128 v[178:181], v242 offset:32768
	ds_read_b128 v[182:185], v242 offset:33792
	ds_read_b128 v[186:189], v242 offset:34816
	ds_read_b128 v[190:193], v242 offset:35840
	ds_read_b128 v[194:197], v242 offset:36864
	ds_read_b128 v[198:201], v242 offset:37888
	ds_read_b128 v[202:205], v242 offset:38912
	ds_read_b128 v[206:209], v242 offset:39936
	global_load_lds_dwordx4 v[218:219], off
	v_lshl_add_u64 v[218:219], s[50:51], 0, v[138:139]
	s_mov_b32 m0, s65
	s_nop 0
	global_load_lds_dwordx4 v[218:219], off
	s_waitcnt vmcnt(8)
	s_waitcnt lgkmcnt(0)
	s_barrier
	s_setprio 1
	s_waitcnt lgkmcnt(0)
	v_mfma_f32_16x16x32_bf16 v[124:127], v[146:149], v[178:181], v[124:127]
	v_mfma_f32_16x16x32_bf16 v[120:123], v[154:157], v[178:181], v[120:123]
	v_mfma_f32_16x16x32_bf16 v[116:119], v[146:149], v[186:189], v[116:119]
	v_mfma_f32_16x16x32_bf16 v[112:115], v[154:157], v[186:189], v[112:115]
	v_mfma_f32_16x16x32_bf16 v[108:111], v[146:149], v[194:197], v[108:111]
	v_mfma_f32_16x16x32_bf16 v[100:103], v[154:157], v[194:197], v[100:103]
	v_mfma_f32_16x16x32_bf16 v[92:95], v[146:149], v[202:205], v[92:95]
	v_mfma_f32_16x16x32_bf16 v[84:87], v[154:157], v[202:205], v[84:87]
	v_mfma_f32_16x16x32_bf16 v[124:127], v[150:153], v[182:185], v[124:127]
	v_mfma_f32_16x16x32_bf16 v[120:123], v[158:161], v[182:185], v[120:123]
	v_mfma_f32_16x16x32_bf16 v[116:119], v[150:153], v[190:193], v[116:119]
	v_mfma_f32_16x16x32_bf16 v[112:115], v[158:161], v[190:193], v[112:115]
	v_mfma_f32_16x16x32_bf16 v[108:111], v[150:153], v[198:201], v[108:111]
	v_mfma_f32_16x16x32_bf16 v[100:103], v[158:161], v[198:201], v[100:103]
	v_mfma_f32_16x16x32_bf16 v[92:95], v[150:153], v[206:209], v[92:95]
	v_mfma_f32_16x16x32_bf16 v[84:87], v[158:161], v[206:209], v[84:87]
	s_setprio 0
	s_setprio 1
	v_mfma_f32_16x16x32_bf16 v[104:107], v[162:165], v[178:181], v[104:107]
	v_mfma_f32_16x16x32_bf16 v[96:99], v[170:173], v[178:181], v[96:99]
	v_mfma_f32_16x16x32_bf16 v[88:91], v[162:165], v[186:189], v[88:91]
	v_mfma_f32_16x16x32_bf16 v[80:83], v[170:173], v[186:189], v[80:83]
	v_mfma_f32_16x16x32_bf16 v[76:79], v[162:165], v[194:197], v[76:79]
	v_mfma_f32_16x16x32_bf16 v[72:75], v[170:173], v[194:197], v[72:75]
	v_mfma_f32_16x16x32_bf16 v[68:71], v[162:165], v[202:205], v[68:71]
	v_mfma_f32_16x16x32_bf16 v[64:67], v[170:173], v[202:205], v[64:67]
	v_mfma_f32_16x16x32_bf16 v[104:107], v[166:169], v[182:185], v[104:107]
	v_mfma_f32_16x16x32_bf16 v[96:99], v[174:177], v[182:185], v[96:99]
	v_mfma_f32_16x16x32_bf16 v[88:91], v[166:169], v[190:193], v[88:91]
	v_mfma_f32_16x16x32_bf16 v[80:83], v[174:177], v[190:193], v[80:83]
	v_mfma_f32_16x16x32_bf16 v[76:79], v[166:169], v[198:201], v[76:79]
	v_mfma_f32_16x16x32_bf16 v[72:75], v[174:177], v[198:201], v[72:75]
	v_mfma_f32_16x16x32_bf16 v[68:71], v[166:169], v[206:209], v[68:71]
	v_mfma_f32_16x16x32_bf16 v[64:67], v[174:177], v[206:209], v[64:67]
	s_setprio 0
	s_barrier
; #define PG8_STAGE(bufoff, gbase, o0, o1) do { \
;         __builtin_amdgcn_global_load_lds((const unsigned*)((const char*)(gbase) + (o0)), (LAS unsigned*)(lds + (bufoff) + ldsw), 16, 0, 0); \
;         __builtin_amdgcn_global_load_lds((const unsigned*)((const char*)(gbase) + (o1)), (LAS unsigned*)(lds + (bufoff) + ldsw + 8192), 16, 0, 0); } while (0)
; #define PG8_LDA(dst, b, h) do { _Pragma("unroll") for (int m = 0; m < 4; ++m) _Pragma("unroll") for (int k = 0; k < 2; ++k) dst[m][k] = *(const LAS bf16x8*)(lds + PG8_SA(b, h) + aoff + m * 2048 + k * 1024); } while (0)
; #define PG8_WAIT_V(n) asm volatile("s_waitcnt vmcnt(" #n ")" ::: "memory")
; #define PG8_WAIT_L(n) asm volatile("s_waitcnt lgkmcnt(" #n ")" ::: "memory")
; #define PG8_BAR __builtin_amdgcn_s_barrier()
; #define PG8_SCHED __builtin_amdgcn_sched_barrier(0)
; template <class Epi, class Sched, class Prob>
; __device__ __forceinline__ void gemm_phase(LAS unsigned char* lds, LAS unsigned char* lds_epi, const Prob g, const Sched& S, const Epi& E, int wid) {
;     ...
;             PG8_LDA(At, 1, 1); PG8_STAGE(PG8_SB(1, 0), b3, vB0, vB1); PG8_STAGE(PG8_SB(1, 1), b3 + hstepB, vB0, vB1); PG8_STAGE(PG8_SA(1, 0), a3, cA00, cA01);
;             PG8_WAIT_V(8); PG8_WAIT_L(0); PG8_BAR; PG8_MMA(1, 0, At, B0); PG8_MMA(1, 1, At, B1); PG8_BAR; PG8_SCHED;
;         }
	s_add_i32 s10, s10, s97
	v_lshl_add_u64 v[210:211], v[210:211], 0, s[24:25]
	s_mov_b32 m0, s10
	ds_read_b128 v[178:181], v242 offset:49152
	ds_read_b128 v[182:185], v242 offset:50176
	ds_read_b128 v[186:189], v242 offset:51200
	ds_read_b128 v[190:193], v242 offset:52224
	ds_read_b128 v[194:197], v242 offset:53248
	ds_read_b128 v[198:201], v242 offset:54272
	ds_read_b128 v[202:205], v242 offset:55296
	ds_read_b128 v[206:209], v242 offset:56320
	global_load_lds_dwordx4 v[210:211], off
	s_add_i32 m0, s10, 0x2000
	s_add_u32 s10, s48, 0x80080
	v_lshl_add_u64 v[210:211], v[212:213], 0, s[24:25]
	s_addc_u32 s11, s49, 0
	s_add_i32 s48, s88, s97
	global_load_lds_dwordx4 v[210:211], off
	v_lshl_add_u64 v[210:211], s[10:11], 0, v[128:129]
	s_mov_b32 m0, s48
	s_nop 0
	global_load_lds_dwordx4 v[210:211], off
	v_lshl_add_u64 v[210:211], s[10:11], 0, v[130:131]
	s_add_i32 m0, s48, 0x2000
	s_nop 0
	global_load_lds_dwordx4 v[210:211], off
	v_lshl_add_u64 v[210:211], v[214:215], 0, s[24:25]
	s_mov_b32 m0, s78
	s_nop 0
	global_load_lds_dwordx4 v[210:211], off
	v_lshl_add_u64 v[210:211], v[216:217], 0, s[24:25]
	s_mov_b32 m0, s79
	s_nop 0
	global_load_lds_dwordx4 v[210:211], off
	s_waitcnt vmcnt(8)
	s_waitcnt lgkmcnt(0)
	s_barrier
	s_setprio 1
	s_waitcnt lgkmcnt(0)
	v_mfma_f32_16x16x32_bf16 v[60:63], v[146:149], v[178:181], v[60:63]
	v_mfma_f32_16x16x32_bf16 v[56:59], v[154:157], v[178:181], v[56:59]
	v_mfma_f32_16x16x32_bf16 v[52:55], v[146:149], v[186:189], v[52:55]
	v_mfma_f32_16x16x32_bf16 v[48:51], v[154:157], v[186:189], v[48:51]
	v_mfma_f32_16x16x32_bf16 v[36:39], v[146:149], v[194:197], v[36:39]
	v_mfma_f32_16x16x32_bf16 v[32:35], v[154:157], v[194:197], v[32:35]
	v_mfma_f32_16x16x32_bf16 v[20:23], v[146:149], v[202:205], v[20:23]
	v_mfma_f32_16x16x32_bf16 v[16:19], v[154:157], v[202:205], v[16:19]
	v_mfma_f32_16x16x32_bf16 v[60:63], v[150:153], v[182:185], v[60:63]
	v_mfma_f32_16x16x32_bf16 v[56:59], v[158:161], v[182:185], v[56:59]
	v_mfma_f32_16x16x32_bf16 v[52:55], v[150:153], v[190:193], v[52:55]
	v_mfma_f32_16x16x32_bf16 v[48:51], v[158:161], v[190:193], v[48:51]
	v_mfma_f32_16x16x32_bf16 v[36:39], v[150:153], v[198:201], v[36:39]
	v_mfma_f32_16x16x32_bf16 v[32:35], v[158:161], v[198:201], v[32:35]
	v_mfma_f32_16x16x32_bf16 v[20:23], v[150:153], v[206:209], v[20:23]
	v_mfma_f32_16x16x32_bf16 v[16:19], v[158:161], v[206:209], v[16:19]
	s_setprio 0
	s_setprio 1
	v_mfma_f32_16x16x32_bf16 v[44:47], v[162:165], v[178:181], v[44:47]
	v_mfma_f32_16x16x32_bf16 v[40:43], v[170:173], v[178:181], v[40:43]
	v_mfma_f32_16x16x32_bf16 v[28:31], v[162:165], v[186:189], v[28:31]
	v_mfma_f32_16x16x32_bf16 v[24:27], v[170:173], v[186:189], v[24:27]
	v_mfma_f32_16x16x32_bf16 v[12:15], v[162:165], v[194:197], v[12:15]
	v_mfma_f32_16x16x32_bf16 v[8:11], v[170:173], v[194:197], v[8:11]
	v_mfma_f32_16x16x32_bf16 v[4:7], v[162:165], v[202:205], v[4:7]
	v_mfma_f32_16x16x32_bf16 v[0:3], v[170:173], v[202:205], v[0:3]
	v_mfma_f32_16x16x32_bf16 v[44:47], v[166:169], v[182:185], v[44:47]
	v_mfma_f32_16x16x32_bf16 v[40:43], v[174:177], v[182:185], v[40:43]
	v_mfma_f32_16x16x32_bf16 v[28:31], v[166:169], v[190:193], v[28:31]
	v_mfma_f32_16x16x32_bf16 v[24:27], v[174:177], v[190:193], v[24:27]
	v_mfma_f32_16x16x32_bf16 v[12:15], v[166:169], v[198:201], v[12:15]
	v_mfma_f32_16x16x32_bf16 v[8:11], v[174:177], v[198:201], v[8:11]
	v_mfma_f32_16x16x32_bf16 v[4:7], v[166:169], v[206:209], v[4:7]
	v_mfma_f32_16x16x32_bf16 v[0:3], v[174:177], v[206:209], v[0:3]
	s_setprio 0
	s_barrier
	s_add_i32 s87, s87, 2
	s_add_u32 s54, s54, 0x100
	s_addc_u32 s55, s55, 0
	s_cmp_gt_u32 s87, 29
	s_mov_b64 s[10:11], s[46:47]

; __host__ __device__ __forceinline__ int perm_a64(int r) { return (r & ~63) + 4 * (r & 15) + ((r >> 4) & 3); }
; #define PG8_STAGE(bufoff, gbase, o0, o1) do { \
;         __builtin_amdgcn_global_load_lds((const unsigned*)((const char*)(gbase) + (o0)), (LAS unsigned*)(lds + (bufoff) + ldsw), 16, 0, 0); \
;         __builtin_amdgcn_global_load_lds((const unsigned*)((const char*)(gbase) + (o1)), (LAS unsigned*)(lds + (bufoff) + ldsw + 8192), 16, 0, 0); } while (0)
; #define PG8_WAIT_V(n) asm volatile("s_waitcnt vmcnt(" #n ")" ::: "memory")
; #define PG8_BAR __builtin_amdgcn_s_barrier()
; #define PG8_ACC_INIT(unit) do { if constexpr (Epi::ACC_INIT) { E.init(acc, unit, wr, wc, fr, fq); } else { \
;         _Pragma("unroll") for (int a = 0; a < 2; ++a) _Pragma("unroll") for (int b = 0; b < 2; ++b) _Pragma("unroll") for (int m = 0; m < 4; ++m) _Pragma("unroll") for (int n = 0; n < 2; ++n) acc[a][b][m][n] = (f32x4){0.f, 0.f, 0.f, 0.f}; } } while (0)
; template <class Epi, class Sched, class Prob>
; __device__ __forceinline__ void gemm_phase(LAS unsigned char* lds, LAS unsigned char* lds_epi, const Prob g, const Sched& S, const Epi& E, int wid) {
;     ...
;     Unit cur, nxt; int ui = 0; int epi_pm = -1;
;     if (!S.next(0, cur)) return;
;     const int Ra0 = aperm_of<Epi>::v ? perm_a64(R0) : R0, Ra1 = aperm_of<Epi>::v ? perm_a64(R1) : R1;
;     const unsigned cA00 = (unsigned)Ra0 * lda2 + (unsigned)C0 * 2u, cA01 = (unsigned)Ra1 * lda2 + (unsigned)C1 * 2u, cA10 = cA00 + (unsigned)HALF * lda2, cA11 = cA01 + (unsigned)HALF * lda2;
;     f32x4 acc[2][2][4][2];
;     ...
;     PG8_ACC_INIT(cur);
;     bf16x8 At[4][2], B0[2][2], B1[2][2];
;     const char* cA = g.a_base(cur); const char* cB = g.b_base(cur);
;     PG8_STAGE(PG8_SB(0, 0), cB, vB0, vB1); PG8_STAGE(PG8_SB(0, 1), cB + hstepB, vB0, vB1); PG8_STAGE(PG8_SA(0, 0), cA, cA00, cA01); PG8_STAGE(PG8_SA(0, 1), cA, cA10, cA11);
;     if (wr == 1) PG8_BAR;
;     PG8_WAIT_V(2); PG8_BAR;
;     PG8_STAGE(PG8_SB(1, 0), cB + kstep, vB0, vB1); PG8_STAGE(PG8_SA(1, 0), cA + kstep, cA00, cA01); PG8_STAGE(PG8_SB(1, 1), cB + hstepB + kstep, vB0, vB1);
;     PG8_WAIT_V(6); PG8_BAR;
.LBB0_1583:
	v_readlane_b32 s20, v254, 24
	s_lshr_b32 s17, s38, 3
	s_lshl_b32 s19, s20, 13
	s_add_u32 s44, s14, 0x350000
	s_addc_u32 s45, s15, 0
	s_add_u32 s46, s14, 0x45000000
	s_addc_u32 s47, s15, 0
	s_add_u32 s48, s14, 0x5d000000
	s_addc_u32 s49, s15, 0
	s_add_u32 s50, s14, 0x800000
	s_addc_u32 s51, s15, 0
	v_readlane_b32 s12, v254, 4
	v_readlane_b32 s13, v254, 5
	s_add_u32 s52, s12, 0xc000
	s_mov_b64 s[54:55], 0x80
	s_addc_u32 s53, s13, 0
	v_lshl_add_u64 v[4:5], v[4:5], 0, s[54:55]
	s_add_i32 m0, s77, 0x18000
	s_lshl_b32 s82, s20, 7
	s_waitcnt vmcnt(2)
	s_barrier
	global_load_lds_dwordx4 v[4:5], off
	v_lshl_add_u64 v[2:3], v[2:3], 0, s[54:55]
	s_add_i32 m0, s77, 0x1a000
	s_add_i32 s83, s77, 0x8000
	s_add_i32 s84, s77, 0xa000
	global_load_lds_dwordx4 v[2:3], off
	v_lshl_add_u64 v[0:1], v[0:1], 0, s[54:55]
	s_mov_b32 m0, s83
	s_add_u32 s12, s10, 0x10080
	global_load_lds_dwordx4 v[0:1], off
	v_lshl_add_u64 v[0:1], v[6:7], 0, s[54:55]
	s_mov_b32 m0, s84
	s_addc_u32 s13, s11, 0
	global_load_lds_dwordx4 v[0:1], off
	v_lshl_add_u64 v[0:1], s[12:13], 0, v[152:153]
	s_add_i32 m0, s77, 0x1c000
	v_ashrrev_i32_e32 v2, 6, v218
	global_load_lds_dwordx4 v[0:1], off
	v_lshl_add_u64 v[0:1], s[12:13], 0, v[154:155]
	s_add_i32 m0, s77, 0x1e000
	v_readlane_b32 s12, v254, 16
	global_load_lds_dwordx4 v[0:1], off
	v_and_b32_e32 v0, 15, v218
	v_or_b32_e32 v1, s12, v0
	v_lshlrev_b32_e32 v3, 6, v1
	v_and_b32_e32 v4, 48, v218
	s_movk_i32 s12, 0x3c0
	v_lshlrev_b32_e32 v1, 2, v1
	v_and_or_b32 v3, v3, s12, v4
	v_lshl_add_u32 v5, v2, 10, s19
	v_and_b32_e32 v1, 32, v1
	v_bitop3_b32 v1, v3, v5, v1 bitop3:0xde
	v_lshlrev_b32_e32 v3, 2, v218
	v_lshl_or_b32 v0, v0, 6, v4
	v_add_lshl_u32 v2, v2, s17, 10
	v_and_b32_e32 v3, 32, v3
	s_waitcnt vmcnt(0)
	v_bitop3_b32 v220, v0, v2, v3 bitop3:0xde
	s_add_i32 s85, 0, 0x10000
	s_add_i32 s86, 0, 0x14000
	v_mov_b32_e32 v159, v153
	v_mov_b32_e32 v163, v153
	v_add_u32_e32 v221, s85, v220
	v_add_u32_e32 v222, s86, v220
	v_add_u32_e32 v223, 0, v1
	s_mov_b32 s56, 0xc1000000
	v_mov_b32_e32 v224, 0x3d2aaaab
	s_mov_b32 s87, 0xbe99999a
	s_mov_b64 s[58:59], 0x800
	s_mov_b64 s[60:61], 0x3e800
	v_mov_b64_e32 v[164:165], 0x3ff
	s_barrier
	s_branch .LBB0_1586

; #define PG8_STAGE(bufoff, gbase, o0, o1) do { \
;         __builtin_amdgcn_global_load_lds((const unsigned*)((const char*)(gbase) + (o0)), (LAS unsigned*)(lds + (bufoff) + ldsw), 16, 0, 0); \
;         __builtin_amdgcn_global_load_lds((const unsigned*)((const char*)(gbase) + (o1)), (LAS unsigned*)(lds + (bufoff) + ldsw + 8192), 16, 0, 0); } while (0)
; #define PG8_LDA(dst, b, h) do { _Pragma("unroll") for (int m = 0; m < 4; ++m) _Pragma("unroll") for (int k = 0; k < 2; ++k) dst[m][k] = *(const LAS bf16x8*)(lds + PG8_SA(b, h) + aoff + m * 2048 + k * 1024); } while (0)
; #define PG8_LDB(dst, b, h) do { _Pragma("unroll") for (int n = 0; n < 2; ++n) _Pragma("unroll") for (int k = 0; k < 2; ++k) dst[n][k] = *(const LAS bf16x8*)(lds + PG8_SB(b, h) + boff + n * 2048 + k * 1024); } while (0)
; #define PG8_WAIT_V(n) asm volatile("s_waitcnt vmcnt(" #n ")" ::: "memory")
; #define PG8_WAIT_L(n) asm volatile("s_waitcnt lgkmcnt(" #n ")" ::: "memory")
; #define PG8_BAR __builtin_amdgcn_s_barrier()
; #define PG8_SCHED __builtin_amdgcn_sched_barrier(0)
; template <class Epi, class Sched, class Prob>
; __device__ __forceinline__ void gemm_phase(LAS unsigned char* lds, LAS unsigned char* lds_epi, const Prob g, const Sched& S, const Epi& E, int wid) {
;     ...
;     for (;;) {
;         const bool has_next = S.next(ui + 1, nxt);
;         const char* nA = has_next ? g.a_base(nxt) : cA; const char* nB = has_next ? g.b_base(nxt) : cB;
; _Pragma("clang loop unroll(disable)")
;         for (int t = 0; t < nt; t += 2) {
;             const bool last = (t == nt - 2);
;             const char* a1 = cA + (size_t)(t + 1) * kstep;
;             const char* a2 = last ? nA : cA + (size_t)(t + 2) * kstep; const char* b2 = last ? nB : cB + (size_t)(t + 2) * kstep;
;             const char* a3 = a2 + kstep; const char* b3 = b2 + kstep;
;             PG8_LDB(B0, 0, 0); PG8_LDB(B1, 0, 1); PG8_SCHED; PG8_LDA(At, 0, 0); PG8_STAGE(PG8_SA(1, 1), a1, cA10, cA11);
;             PG8_WAIT_V(8); PG8_WAIT_L(0); PG8_BAR; PG8_MMA(0, 0, At, B0); PG8_MMA(0, 1, At, B1); PG8_BAR; PG8_SCHED;
;             PG8_LDA(At, 0, 1); PG8_STAGE(PG8_SB(0, 0), b2, vB0, vB1); PG8_STAGE(PG8_SB(0, 1), b2 + hstepB, vB0, vB1); PG8_STAGE(PG8_SA(0, 0), a2, cA00, cA01);
;             PG8_WAIT_V(8); PG8_WAIT_L(0); PG8_BAR; PG8_MMA(1, 0, At, B0); PG8_MMA(1, 1, At, B1); PG8_BAR; PG8_SCHED;
.LBB0_1594:
	s_ashr_i32 s65, s64, 31
	s_lshl_b64 s[14:15], s[64:65], 20
	s_add_u32 s17, s40, s14
	s_addc_u32 s19, s41, s15
	s_ashr_i32 s14, s62, 1
	s_ashr_i32 s15, s14, 31
	s_lshl_b64 s[14:15], s[14:15], 9
	s_add_u32 s68, s17, s14
	s_addc_u32 s69, s19, s15
	s_and_b64 s[14:15], s[66:67], exec
	s_cselect_b32 s17, s69, s9
	s_cselect_b32 s19, s68, s8
	s_ashr_i32 s63, s62, 31
	s_lshl_b64 s[14:15], s[62:63], 17
	s_add_u32 s70, s33, s14
	s_addc_u32 s71, s76, s15
	s_and_b64 s[14:15], s[66:67], exec
	v_mov_b32_e32 v0, 0
	s_cselect_b32 s26, s71, s11
	s_cselect_b32 s27, s70, s10
	s_mov_b64 s[20:21], -1
	s_mov_b64 s[14:15], 0
	s_add_u32 s24, s8, s14
	s_addc_u32 s25, s9, s15
	s_add_u32 s22, s24, 0x100
	s_addc_u32 s23, s25, 0
	v_cndmask_b32_e64 v56, 0, 1, s[20:21]
	s_and_b64 s[20:21], s[12:13], exec
	s_cselect_b32 s20, s19, s22
	s_cselect_b32 s21, s17, s23
	s_add_u32 s14, s10, s14
	s_addc_u32 s15, s11, s15
	s_add_u32 s14, s14, 0x100
	v_cmp_ne_u32_e32 vcc, 1, v56
	ds_read_b128 v[56:59], v221
	ds_read_b128 v[68:71], v221 offset:1024
	ds_read_b128 v[72:75], v221 offset:2048
	ds_read_b128 v[88:91], v221 offset:3072
	ds_read_b128 v[100:103], v222
	ds_read_b128 v[104:107], v222 offset:1024
	ds_read_b128 v[166:169], v222 offset:2048
	ds_read_b128 v[170:173], v222 offset:3072
	s_addc_u32 s15, s15, 0
	s_and_b64 s[12:13], s[12:13], exec
	s_cselect_b32 s15, s26, s15
	s_cselect_b32 s14, s27, s14
	s_add_i32 s65, s85, s97
	s_add_i32 m0, s77, 0xc000
	s_add_i32 s72, s77, 0xe000
	s_add_i32 s36, s65, 0x2000
	s_add_u32 s22, s14, 0x10000
	s_addc_u32 s23, s15, 0
	s_add_i32 s35, 0, 0x18000
	s_add_i32 s63, s86, s97
	s_add_i32 s31, s35, s97
	s_add_i32 s37, s63, 0x2000
	s_add_i32 s34, 0, 0x1c000
	s_add_i32 s29, s31, 0x2000
	s_add_u32 s12, s14, 0x10080
	s_addc_u32 s13, s15, 0
	s_add_i32 s30, s34, s97
	s_add_i32 s28, s30, 0x2000
	v_lshl_add_u64 v[206:207], s[24:25], 0, v[158:159]
	v_lshl_add_u64 v[206:207], v[206:207], 0, s[54:55]
	ds_read_b128 v[174:177], v223
	ds_read_b128 v[178:181], v223 offset:1024
	ds_read_b128 v[182:185], v223 offset:2048
	ds_read_b128 v[186:189], v223 offset:3072
	ds_read_b128 v[190:193], v223 offset:4096
	ds_read_b128 v[194:197], v223 offset:5120
	ds_read_b128 v[198:201], v223 offset:6144
	ds_read_b128 v[202:205], v223 offset:7168
	global_load_lds_dwordx4 v[206:207], off
	v_lshl_add_u64 v[206:207], s[24:25], 0, v[162:163]
	v_lshl_add_u64 v[206:207], v[206:207], 0, s[54:55]
	s_mov_b32 m0, s72
	s_nop 0
	global_load_lds_dwordx4 v[206:207], off
	s_waitcnt vmcnt(56)
	s_waitcnt lgkmcnt(0)
	s_barrier
	s_setprio 1
	s_waitcnt lgkmcnt(0)
	v_mfma_f32_16x16x32_bf16 v[148:151], v[56:59], v[174:177], 0
	v_mfma_f32_16x16x32_bf16 v[116:119], v[72:75], v[174:177], 0
	v_mfma_f32_16x16x32_bf16 v[144:147], v[56:59], v[182:185], 0
	v_mfma_f32_16x16x32_bf16 v[112:115], v[72:75], v[182:185], 0
	v_mfma_f32_16x16x32_bf16 v[140:143], v[56:59], v[190:193], 0
	v_mfma_f32_16x16x32_bf16 v[108:111], v[72:75], v[190:193], 0
	v_mfma_f32_16x16x32_bf16 v[136:139], v[56:59], v[198:201], 0
	v_mfma_f32_16x16x32_bf16 v[96:99], v[72:75], v[198:201], 0
	v_mfma_f32_16x16x32_bf16 v[148:151], v[68:71], v[178:181], v[148:151]
	v_mfma_f32_16x16x32_bf16 v[116:119], v[88:91], v[178:181], v[116:119]
	v_mfma_f32_16x16x32_bf16 v[144:147], v[68:71], v[186:189], v[144:147]
	v_mfma_f32_16x16x32_bf16 v[112:115], v[88:91], v[186:189], v[112:115]
	v_mfma_f32_16x16x32_bf16 v[140:143], v[68:71], v[194:197], v[140:143]
	v_mfma_f32_16x16x32_bf16 v[108:111], v[88:91], v[194:197], v[108:111]
	v_mfma_f32_16x16x32_bf16 v[136:139], v[68:71], v[202:205], v[136:139]
	v_mfma_f32_16x16x32_bf16 v[96:99], v[88:91], v[202:205], v[96:99]
	s_setprio 0
	s_setprio 1
	v_mfma_f32_16x16x32_bf16 v[132:135], v[100:103], v[174:177], 0
	v_mfma_f32_16x16x32_bf16 v[92:95], v[166:169], v[174:177], 0
	v_mfma_f32_16x16x32_bf16 v[128:131], v[100:103], v[182:185], 0
	v_mfma_f32_16x16x32_bf16 v[84:87], v[166:169], v[182:185], 0
	v_mfma_f32_16x16x32_bf16 v[124:127], v[100:103], v[190:193], 0
	v_mfma_f32_16x16x32_bf16 v[80:83], v[166:169], v[190:193], 0
	v_mfma_f32_16x16x32_bf16 v[120:123], v[100:103], v[198:201], 0
	v_mfma_f32_16x16x32_bf16 v[76:79], v[166:169], v[198:201], 0
	v_mfma_f32_16x16x32_bf16 v[132:135], v[104:107], v[178:181], v[132:135]
	v_mfma_f32_16x16x32_bf16 v[92:95], v[170:173], v[178:181], v[92:95]
	v_mfma_f32_16x16x32_bf16 v[128:131], v[104:107], v[186:189], v[128:131]
	v_mfma_f32_16x16x32_bf16 v[84:87], v[170:173], v[186:189], v[84:87]
	v_mfma_f32_16x16x32_bf16 v[124:127], v[104:107], v[194:197], v[124:127]
	v_mfma_f32_16x16x32_bf16 v[80:83], v[170:173], v[194:197], v[80:83]
	v_mfma_f32_16x16x32_bf16 v[120:123], v[104:107], v[202:205], v[120:123]
	v_mfma_f32_16x16x32_bf16 v[76:79], v[170:173], v[202:205], v[76:79]
	s_setprio 0
	s_barrier
	s_mov_b32 m0, s65
	v_lshl_add_u64 v[206:207], s[14:15], 0, v[152:153]
	ds_read_b128 v[174:177], v223 offset:16384
	ds_read_b128 v[178:181], v223 offset:17408
	ds_read_b128 v[182:185], v223 offset:18432
	ds_read_b128 v[186:189], v223 offset:19456
	ds_read_b128 v[190:193], v223 offset:20480
	ds_read_b128 v[194:197], v223 offset:21504
	ds_read_b128 v[198:201], v223 offset:22528
	ds_read_b128 v[202:205], v223 offset:23552
	global_load_lds_dwordx4 v[206:207], off
	v_lshl_add_u64 v[208:209], s[14:15], 0, v[154:155]
	s_mov_b32 m0, s36
	v_lshl_add_u64 v[210:211], s[22:23], 0, v[152:153]
	global_load_lds_dwordx4 v[208:209], off
	s_mov_b32 m0, s63
	v_lshl_add_u64 v[212:213], s[20:21], 0, v[160:161]
	global_load_lds_dwordx4 v[210:211], off
	v_lshl_add_u64 v[210:211], s[22:23], 0, v[154:155]
	s_mov_b32 m0, s37
	s_nop 0
	global_load_lds_dwordx4 v[210:211], off
	v_lshl_add_u64 v[210:211], s[20:21], 0, v[156:157]
	s_mov_b32 m0, s77
	s_nop 0
	global_load_lds_dwordx4 v[210:211], off
	s_mov_b32 m0, s78
	s_nop 0
	global_load_lds_dwordx4 v[212:213], off
	s_waitcnt vmcnt(56)
	s_waitcnt lgkmcnt(0)
	s_barrier
; #define PG8_STAGE(bufoff, gbase, o0, o1) do { \
;         __builtin_amdgcn_global_load_lds((const unsigned*)((const char*)(gbase) + (o0)), (LAS unsigned*)(lds + (bufoff) + ldsw), 16, 0, 0); \
;         __builtin_amdgcn_global_load_lds((const unsigned*)((const char*)(gbase) + (o1)), (LAS unsigned*)(lds + (bufoff) + ldsw + 8192), 16, 0, 0); } while (0)
; #define PG8_LDA(dst, b, h) do { _Pragma("unroll") for (int m = 0; m < 4; ++m) _Pragma("unroll") for (int k = 0; k < 2; ++k) dst[m][k] = *(const LAS bf16x8*)(lds + PG8_SA(b, h) + aoff + m * 2048 + k * 1024); } while (0)
; #define PG8_LDB(dst, b, h) do { _Pragma("unroll") for (int n = 0; n < 2; ++n) _Pragma("unroll") for (int k = 0; k < 2; ++k) dst[n][k] = *(const LAS bf16x8*)(lds + PG8_SB(b, h) + boff + n * 2048 + k * 1024); } while (0)
; #define PG8_WAIT_V(n) asm volatile("s_waitcnt vmcnt(" #n ")" ::: "memory")
; #define PG8_WAIT_L(n) asm volatile("s_waitcnt lgkmcnt(" #n ")" ::: "memory")
; #define PG8_BAR __builtin_amdgcn_s_barrier()
; #define PG8_SCHED __builtin_amdgcn_sched_barrier(0)
; template <class Epi, class Sched, class Prob>
; __device__ __forceinline__ void gemm_phase(LAS unsigned char* lds, LAS unsigned char* lds_epi, const Prob g, const Sched& S, const Epi& E, int wid) {
;     ...
;             PG8_WAIT_V(8); PG8_WAIT_L(0); PG8_BAR; PG8_MMA(0, 0, At, B0); PG8_MMA(0, 1, At, B1); PG8_BAR; PG8_SCHED;
;             PG8_LDA(At, 0, 1); PG8_STAGE(PG8_SB(0, 0), b2, vB0, vB1); PG8_STAGE(PG8_SB(0, 1), b2 + hstepB, vB0, vB1); PG8_STAGE(PG8_SA(0, 0), a2, cA00, cA01);
;             PG8_WAIT_V(8); PG8_WAIT_L(0); PG8_BAR; PG8_MMA(1, 0, At, B0); PG8_MMA(1, 1, At, B1); PG8_BAR; PG8_SCHED;
;             PG8_LDB(B0, 1, 0); PG8_LDB(B1, 1, 1); PG8_SCHED; PG8_LDA(At, 1, 0); PG8_STAGE(PG8_SA(0, 1), a2, cA10, cA11);
;             PG8_WAIT_V(8); PG8_WAIT_L(0); PG8_BAR; PG8_MMA(0, 0, At, B0); PG8_MMA(0, 1, At, B1); PG8_BAR; PG8_SCHED;
;             PG8_LDA(At, 1, 1); PG8_STAGE(PG8_SB(1, 0), b3, vB0, vB1); PG8_STAGE(PG8_SB(1, 1), b3 + hstepB, vB0, vB1); PG8_STAGE(PG8_SA(1, 0), a3, cA00, cA01);
	s_setprio 1
	s_waitcnt lgkmcnt(0)
	v_mfma_f32_16x16x32_bf16 v[64:67], v[56:59], v[174:177], 0
	v_mfma_f32_16x16x32_bf16 v[28:31], v[72:75], v[174:177], 0
	v_mfma_f32_16x16x32_bf16 v[60:63], v[56:59], v[182:185], 0
	v_mfma_f32_16x16x32_bf16 v[24:27], v[72:75], v[182:185], 0
	v_mfma_f32_16x16x32_bf16 v[52:55], v[56:59], v[190:193], 0
	v_mfma_f32_16x16x32_bf16 v[20:23], v[72:75], v[190:193], 0
	v_mfma_f32_16x16x32_bf16 v[48:51], v[56:59], v[198:201], 0
	v_mfma_f32_16x16x32_bf16 v[16:19], v[72:75], v[198:201], 0
	v_mfma_f32_16x16x32_bf16 v[64:67], v[68:71], v[178:181], v[64:67]
	v_mfma_f32_16x16x32_bf16 v[28:31], v[88:91], v[178:181], v[28:31]
	v_mfma_f32_16x16x32_bf16 v[60:63], v[68:71], v[186:189], v[60:63]
	v_mfma_f32_16x16x32_bf16 v[24:27], v[88:91], v[186:189], v[24:27]
	v_mfma_f32_16x16x32_bf16 v[52:55], v[68:71], v[194:197], v[52:55]
	v_mfma_f32_16x16x32_bf16 v[20:23], v[88:91], v[194:197], v[20:23]
	v_mfma_f32_16x16x32_bf16 v[48:51], v[68:71], v[202:205], v[48:51]
	v_mfma_f32_16x16x32_bf16 v[16:19], v[88:91], v[202:205], v[16:19]
	s_setprio 0
	s_setprio 1
	v_mfma_f32_16x16x32_bf16 v[44:47], v[100:103], v[174:177], 0
	v_mfma_f32_16x16x32_bf16 v[12:15], v[166:169], v[174:177], 0
	v_mfma_f32_16x16x32_bf16 v[40:43], v[100:103], v[182:185], 0
	v_mfma_f32_16x16x32_bf16 v[8:11], v[166:169], v[182:185], 0
	v_mfma_f32_16x16x32_bf16 v[36:39], v[100:103], v[190:193], 0
	v_mfma_f32_16x16x32_bf16 v[4:7], v[166:169], v[190:193], 0
	v_mfma_f32_16x16x32_bf16 v[32:35], v[100:103], v[198:201], 0
	v_mfma_f32_16x16x32_bf16 v[0:3], v[166:169], v[198:201], 0
	v_mfma_f32_16x16x32_bf16 v[44:47], v[104:107], v[178:181], v[44:47]
	v_mfma_f32_16x16x32_bf16 v[12:15], v[170:173], v[178:181], v[12:15]
	v_mfma_f32_16x16x32_bf16 v[40:43], v[104:107], v[186:189], v[40:43]
	v_mfma_f32_16x16x32_bf16 v[8:11], v[170:173], v[186:189], v[8:11]
	v_mfma_f32_16x16x32_bf16 v[36:39], v[104:107], v[194:197], v[36:39]
	v_mfma_f32_16x16x32_bf16 v[4:7], v[170:173], v[194:197], v[4:7]
	v_mfma_f32_16x16x32_bf16 v[32:35], v[104:107], v[202:205], v[32:35]
	v_mfma_f32_16x16x32_bf16 v[0:3], v[170:173], v[202:205], v[0:3]
	s_setprio 0
	s_barrier
	v_add_u32_e32 v88, s35, v220
	v_add_u32_e32 v170, s34, v220
	ds_read_b128 v[56:59], v88
	ds_read_b128 v[68:71], v88 offset:1024
	ds_read_b128 v[72:75], v88 offset:2048
	ds_read_b128 v[88:91], v88 offset:3072
	ds_read_b128 v[100:103], v170
	ds_read_b128 v[104:107], v170 offset:1024
	ds_read_b128 v[166:169], v170 offset:2048
	ds_read_b128 v[170:173], v170 offset:3072
	s_mov_b32 m0, s79
	v_lshl_add_u64 v[214:215], s[20:21], 0, v[158:159]
	ds_read_b128 v[174:177], v223 offset:32768
	ds_read_b128 v[178:181], v223 offset:33792
	ds_read_b128 v[182:185], v223 offset:34816
	ds_read_b128 v[186:189], v223 offset:35840
	ds_read_b128 v[190:193], v223 offset:36864
	ds_read_b128 v[194:197], v223 offset:37888
	ds_read_b128 v[198:201], v223 offset:38912
	ds_read_b128 v[202:205], v223 offset:39936
	global_load_lds_dwordx4 v[214:215], off
	v_lshl_add_u64 v[214:215], s[20:21], 0, v[162:163]
	s_mov_b32 m0, s80
	s_nop 0
	global_load_lds_dwordx4 v[214:215], off
	s_waitcnt vmcnt(8)
	s_waitcnt lgkmcnt(0)
	s_barrier
	s_setprio 1
	s_waitcnt lgkmcnt(0)
	v_mfma_f32_16x16x32_bf16 v[148:151], v[56:59], v[174:177], v[148:151]
	v_mfma_f32_16x16x32_bf16 v[116:119], v[72:75], v[174:177], v[116:119]
	v_mfma_f32_16x16x32_bf16 v[144:147], v[56:59], v[182:185], v[144:147]
	v_mfma_f32_16x16x32_bf16 v[112:115], v[72:75], v[182:185], v[112:115]
	v_mfma_f32_16x16x32_bf16 v[140:143], v[56:59], v[190:193], v[140:143]
	v_mfma_f32_16x16x32_bf16 v[108:111], v[72:75], v[190:193], v[108:111]
	v_mfma_f32_16x16x32_bf16 v[136:139], v[56:59], v[198:201], v[136:139]
	v_mfma_f32_16x16x32_bf16 v[96:99], v[72:75], v[198:201], v[96:99]
	v_mfma_f32_16x16x32_bf16 v[148:151], v[68:71], v[178:181], v[148:151]
	v_mfma_f32_16x16x32_bf16 v[116:119], v[88:91], v[178:181], v[116:119]
	v_mfma_f32_16x16x32_bf16 v[144:147], v[68:71], v[186:189], v[144:147]
	v_mfma_f32_16x16x32_bf16 v[112:115], v[88:91], v[186:189], v[112:115]
	v_mfma_f32_16x16x32_bf16 v[140:143], v[68:71], v[194:197], v[140:143]
	v_mfma_f32_16x16x32_bf16 v[108:111], v[88:91], v[194:197], v[108:111]
	v_mfma_f32_16x16x32_bf16 v[136:139], v[68:71], v[202:205], v[136:139]
	v_mfma_f32_16x16x32_bf16 v[96:99], v[88:91], v[202:205], v[96:99]
	s_setprio 0
	s_setprio 1
	v_mfma_f32_16x16x32_bf16 v[132:135], v[100:103], v[174:177], v[132:135]
	v_mfma_f32_16x16x32_bf16 v[92:95], v[166:169], v[174:177], v[92:95]
	v_mfma_f32_16x16x32_bf16 v[128:131], v[100:103], v[182:185], v[128:131]
	v_mfma_f32_16x16x32_bf16 v[84:87], v[166:169], v[182:185], v[84:87]
	v_mfma_f32_16x16x32_bf16 v[124:127], v[100:103], v[190:193], v[124:127]
	v_mfma_f32_16x16x32_bf16 v[80:83], v[166:169], v[190:193], v[80:83]
	v_mfma_f32_16x16x32_bf16 v[120:123], v[100:103], v[198:201], v[120:123]
	v_mfma_f32_16x16x32_bf16 v[76:79], v[166:169], v[198:201], v[76:79]
	v_mfma_f32_16x16x32_bf16 v[132:135], v[104:107], v[178:181], v[132:135]
	v_mfma_f32_16x16x32_bf16 v[92:95], v[170:173], v[178:181], v[92:95]
	v_mfma_f32_16x16x32_bf16 v[128:131], v[104:107], v[186:189], v[128:131]
	v_mfma_f32_16x16x32_bf16 v[84:87], v[170:173], v[186:189], v[84:87]
	v_mfma_f32_16x16x32_bf16 v[124:127], v[104:107], v[194:197], v[124:127]
	v_mfma_f32_16x16x32_bf16 v[80:83], v[170:173], v[194:197], v[80:83]
	v_mfma_f32_16x16x32_bf16 v[120:123], v[104:107], v[202:205], v[120:123]
	v_mfma_f32_16x16x32_bf16 v[76:79], v[170:173], v[202:205], v[76:79]
	s_setprio 0
	s_barrier
; #define PG8_STAGE(bufoff, gbase, o0, o1) do { \
;         __builtin_amdgcn_global_load_lds((const unsigned*)((const char*)(gbase) + (o0)), (LAS unsigned*)(lds + (bufoff) + ldsw), 16, 0, 0); \
;         __builtin_amdgcn_global_load_lds((const unsigned*)((const char*)(gbase) + (o1)), (LAS unsigned*)(lds + (bufoff) + ldsw + 8192), 16, 0, 0); } while (0)
; #define PG8_LDA(dst, b, h) do { _Pragma("unroll") for (int m = 0; m < 4; ++m) _Pragma("unroll") for (int k = 0; k < 2; ++k) dst[m][k] = *(const LAS bf16x8*)(lds + PG8_SA(b, h) + aoff + m * 2048 + k * 1024); } while (0)
; #define PG8_WAIT_V(n) asm volatile("s_waitcnt vmcnt(" #n ")" ::: "memory")
; #define PG8_WAIT_L(n) asm volatile("s_waitcnt lgkmcnt(" #n ")" ::: "memory")
; #define PG8_BAR __builtin_amdgcn_s_barrier()
; #define PG8_SCHED __builtin_amdgcn_sched_barrier(0)
; template <class Epi, class Sched, class Prob>
; __device__ __forceinline__ void gemm_phase(LAS unsigned char* lds, LAS unsigned char* lds_epi, const Prob g, const Sched& S, const Epi& E, int wid) {
;     ...
;             PG8_LDA(At, 1, 1); PG8_STAGE(PG8_SB(1, 0), b3, vB0, vB1); PG8_STAGE(PG8_SB(1, 1), b3 + hstepB, vB0, vB1); PG8_STAGE(PG8_SA(1, 0), a3, cA00, cA01);
;             PG8_WAIT_V(8); PG8_WAIT_L(0); PG8_BAR; PG8_MMA(1, 0, At, B0); PG8_MMA(1, 1, At, B1); PG8_BAR; PG8_SCHED;
;         }
	s_mov_b32 m0, s31
	v_lshl_add_u64 v[206:207], v[206:207], 0, s[54:55]
	ds_read_b128 v[174:177], v223 offset:49152
	ds_read_b128 v[178:181], v223 offset:50176
	ds_read_b128 v[182:185], v223 offset:51200
	ds_read_b128 v[186:189], v223 offset:52224
	ds_read_b128 v[190:193], v223 offset:53248
	ds_read_b128 v[194:197], v223 offset:54272
	ds_read_b128 v[198:201], v223 offset:55296
	ds_read_b128 v[202:205], v223 offset:56320
	global_load_lds_dwordx4 v[206:207], off
	v_lshl_add_u64 v[206:207], v[208:209], 0, s[54:55]
	s_mov_b32 m0, s29
	s_nop 0
	global_load_lds_dwordx4 v[206:207], off
	v_lshl_add_u64 v[206:207], s[12:13], 0, v[152:153]
	s_mov_b32 m0, s30
	s_nop 0
	global_load_lds_dwordx4 v[206:207], off
	v_lshl_add_u64 v[206:207], s[12:13], 0, v[154:155]
	s_mov_b32 m0, s28
	s_nop 0
	global_load_lds_dwordx4 v[206:207], off
	v_lshl_add_u64 v[206:207], v[210:211], 0, s[54:55]
	s_mov_b32 m0, s83
	s_nop 0
	global_load_lds_dwordx4 v[206:207], off
	v_lshl_add_u64 v[206:207], v[212:213], 0, s[54:55]
	s_mov_b32 m0, s84
	s_nop 0
	global_load_lds_dwordx4 v[206:207], off
	s_waitcnt vmcnt(8)
	s_waitcnt lgkmcnt(0)
	s_barrier
	s_setprio 1
	s_waitcnt lgkmcnt(0)
	v_mfma_f32_16x16x32_bf16 v[64:67], v[56:59], v[174:177], v[64:67]
	v_mfma_f32_16x16x32_bf16 v[28:31], v[72:75], v[174:177], v[28:31]
	v_mfma_f32_16x16x32_bf16 v[60:63], v[56:59], v[182:185], v[60:63]
	v_mfma_f32_16x16x32_bf16 v[24:27], v[72:75], v[182:185], v[24:27]
	v_mfma_f32_16x16x32_bf16 v[52:55], v[56:59], v[190:193], v[52:55]
	v_mfma_f32_16x16x32_bf16 v[20:23], v[72:75], v[190:193], v[20:23]
	v_mfma_f32_16x16x32_bf16 v[48:51], v[56:59], v[198:201], v[48:51]
	v_mfma_f32_16x16x32_bf16 v[16:19], v[72:75], v[198:201], v[16:19]
	v_mfma_f32_16x16x32_bf16 v[64:67], v[68:71], v[178:181], v[64:67]
	v_mfma_f32_16x16x32_bf16 v[28:31], v[88:91], v[178:181], v[28:31]
	v_mfma_f32_16x16x32_bf16 v[60:63], v[68:71], v[186:189], v[60:63]
	v_mfma_f32_16x16x32_bf16 v[24:27], v[88:91], v[186:189], v[24:27]
	v_mfma_f32_16x16x32_bf16 v[52:55], v[68:71], v[194:197], v[52:55]
	v_mfma_f32_16x16x32_bf16 v[20:23], v[88:91], v[194:197], v[20:23]
	v_mfma_f32_16x16x32_bf16 v[48:51], v[68:71], v[202:205], v[48:51]
	v_mfma_f32_16x16x32_bf16 v[16:19], v[88:91], v[202:205], v[16:19]
	s_setprio 0
	s_setprio 1
	v_mfma_f32_16x16x32_bf16 v[44:47], v[100:103], v[174:177], v[44:47]
	v_mfma_f32_16x16x32_bf16 v[12:15], v[166:169], v[174:177], v[12:15]
	v_mfma_f32_16x16x32_bf16 v[40:43], v[100:103], v[182:185], v[40:43]
	v_mfma_f32_16x16x32_bf16 v[8:11], v[166:169], v[182:185], v[8:11]
	v_mfma_f32_16x16x32_bf16 v[36:39], v[100:103], v[190:193], v[36:39]
	v_mfma_f32_16x16x32_bf16 v[4:7], v[166:169], v[190:193], v[4:7]
	v_mfma_f32_16x16x32_bf16 v[32:35], v[100:103], v[198:201], v[32:35]
	v_mfma_f32_16x16x32_bf16 v[0:3], v[166:169], v[198:201], v[0:3]
	v_mfma_f32_16x16x32_bf16 v[44:47], v[104:107], v[178:181], v[44:47]
	v_mfma_f32_16x16x32_bf16 v[12:15], v[170:173], v[178:181], v[12:15]
	v_mfma_f32_16x16x32_bf16 v[40:43], v[104:107], v[186:189], v[40:43]
	v_mfma_f32_16x16x32_bf16 v[8:11], v[170:173], v[186:189], v[8:11]
	v_mfma_f32_16x16x32_bf16 v[36:39], v[104:107], v[194:197], v[36:39]
	v_mfma_f32_16x16x32_bf16 v[4:7], v[170:173], v[194:197], v[4:7]
	v_mfma_f32_16x16x32_bf16 v[32:35], v[104:107], v[202:205], v[32:35]
	v_mfma_f32_16x16x32_bf16 v[0:3], v[170:173], v[202:205], v[0:3]
	s_setprio 0
	s_barrier
	s_mov_b64 s[20:21], 0
	s_mov_b64 s[12:13], -1
	s_mov_b64 s[14:15], 0x100

; __host__ __device__ __forceinline__ int perm_a64(int r) { return (r & ~63) + 4 * (r & 15) + ((r >> 4) & 3); }
; #define PG8_STAGE(bufoff, gbase, o0, o1) do { \
;         __builtin_amdgcn_global_load_lds((const unsigned*)((const char*)(gbase) + (o0)), (LAS unsigned*)(lds + (bufoff) + ldsw), 16, 0, 0); \
;         __builtin_amdgcn_global_load_lds((const unsigned*)((const char*)(gbase) + (o1)), (LAS unsigned*)(lds + (bufoff) + ldsw + 8192), 16, 0, 0); } while (0)
; #define PG8_WAIT_V(n) asm volatile("s_waitcnt vmcnt(" #n ")" ::: "memory")
; #define PG8_BAR __builtin_amdgcn_s_barrier()
; #define PG8_ACC_INIT(unit) do { if constexpr (Epi::ACC_INIT) { E.init(acc, unit, wr, wc, fr, fq); } else { \
;         _Pragma("unroll") for (int a = 0; a < 2; ++a) _Pragma("unroll") for (int b = 0; b < 2; ++b) _Pragma("unroll") for (int m = 0; m < 4; ++m) _Pragma("unroll") for (int n = 0; n < 2; ++n) acc[a][b][m][n] = (f32x4){0.f, 0.f, 0.f, 0.f}; } } while (0)
; template <class Epi, class Sched, class Prob>
; __device__ __forceinline__ void gemm_phase(LAS unsigned char* lds, LAS unsigned char* lds_epi, const Prob g, const Sched& S, const Epi& E, int wid) {
;     ...
;     Unit cur, nxt; int ui = 0; int epi_pm = -1;
;     if (!S.next(0, cur)) return;
;     const int Ra0 = aperm_of<Epi>::v ? perm_a64(R0) : R0, Ra1 = aperm_of<Epi>::v ? perm_a64(R1) : R1;
;     const unsigned cA00 = (unsigned)Ra0 * lda2 + (unsigned)C0 * 2u, cA01 = (unsigned)Ra1 * lda2 + (unsigned)C1 * 2u, cA10 = cA00 + (unsigned)HALF * lda2, cA11 = cA01 + (unsigned)HALF * lda2;
;     f32x4 acc[2][2][4][2];
;     ...
;     PG8_ACC_INIT(cur);
;     bf16x8 At[4][2], B0[2][2], B1[2][2];
;     const char* cA = g.a_base(cur); const char* cB = g.b_base(cur);
;     PG8_STAGE(PG8_SB(0, 0), cB, vB0, vB1); PG8_STAGE(PG8_SB(0, 1), cB + hstepB, vB0, vB1); PG8_STAGE(PG8_SA(0, 0), cA, cA00, cA01); PG8_STAGE(PG8_SA(0, 1), cA, cA10, cA11);
;     if (wr == 1) PG8_BAR;
;     PG8_WAIT_V(2); PG8_BAR;
;     PG8_STAGE(PG8_SB(1, 0), cB + kstep, vB0, vB1); PG8_STAGE(PG8_SA(1, 0), cA + kstep, cA00, cA01); PG8_STAGE(PG8_SB(1, 1), cB + hstepB + kstep, vB0, vB1);
;     PG8_WAIT_V(6); PG8_BAR;
.LBB0_2082:
	s_add_u32 s14, s6, 0x41000000
	s_addc_u32 s15, s7, 0
	s_add_u32 s16, s6, 0x3fd400
	s_mov_b64 s[18:19], 0x80
	s_addc_u32 s17, s7, 0
	v_lshl_add_u64 v[6:7], v[6:7], 0, s[18:19]
	s_add_i32 m0, s35, 0x18000
	s_waitcnt vmcnt(2)
	s_barrier
	global_load_lds_dwordx4 v[6:7], off
	v_lshl_add_u64 v[4:5], v[4:5], 0, s[18:19]
	s_add_i32 m0, s35, 0x1a000
	s_add_i32 s61, s35, 0x8000
	global_load_lds_dwordx4 v[4:5], off
	v_lshl_add_u64 v[2:3], v[2:3], 0, s[18:19]
	s_mov_b32 m0, s61
	s_add_i32 s62, s35, 0xa000
	global_load_lds_dwordx4 v[2:3], off
	v_lshl_add_u64 v[2:3], v[8:9], 0, s[18:19]
	s_mov_b32 m0, s62
	s_mov_b64 s[20:21], 0x40080
	global_load_lds_dwordx4 v[2:3], off
	v_lshl_add_u64 v[2:3], v[0:1], 0, s[20:21]
	v_lshl_add_u64 v[4:5], v[2:3], 0, v[160:161]
	s_add_i32 m0, s35, 0x1c000
	v_lshl_add_u64 v[2:3], v[2:3], 0, v[162:163]
	global_load_lds_dwordx4 v[4:5], off
	s_add_i32 m0, s35, 0x1e000
	v_readlane_b32 s3, v254, 16
	global_load_lds_dwordx4 v[2:3], off
	v_and_b32_e32 v3, 15, v12
	v_or_b32_e32 v194, s3, v3
	v_ashrrev_i32_e32 v4, 6, v12
	v_lshlrev_b32_e32 v5, 6, v194
	v_and_b32_e32 v6, 48, v12
	s_movk_i32 s3, 0x3c0
	v_lshlrev_b32_e32 v8, 2, v194
	v_and_or_b32 v5, v5, s3, v6
	v_lshl_add_u32 v7, v4, 10, s33
	v_and_b32_e32 v8, 32, v8
	v_ashrrev_i32_e32 v2, 1, v12
	v_bitop3_b32 v5, v5, v7, v8 bitop3:0xde
	v_lshlrev_b32_e32 v7, 2, v3
	v_and_b32_e32 v2, -8, v2
	v_lshl_or_b32 v6, v3, 6, v6
	v_add_lshl_u32 v4, v4, s48, 10
	v_and_b32_e32 v3, 32, v7
	v_bitop3_b32 v195, v6, v4, v3 bitop3:0xde
	v_ashrrev_i32_e32 v3, 31, v2
	v_lshl_add_u64 v[172:173], v[2:3], 0, s[38:39]
	v_lshlrev_b32_e32 v2, 14, v10
	v_and_b32_e32 v2, 0xffff8000, v2
	v_lshl_add_u32 v2, v11, 11, v2
	v_and_b32_e32 v3, 1, v10
	v_lshl_or_b32 v2, v3, 6, v2
	v_lshlrev_b32_e32 v3, 1, v14
	v_add3_u32 v174, v2, v3, s8
	v_lshlrev_b32_e32 v2, 14, v13
	v_and_b32_e32 v2, 0xffff8000, v2
	s_waitcnt vmcnt(0)
	v_add_u32_e32 v196, s91, v12
	s_movk_i32 s3, 0x100
	v_lshl_add_u32 v2, v15, 11, v2
	v_and_b32_e32 v3, 1, v13
	v_cmp_gt_i32_e64 s[6:7], s3, v196
	s_add_i32 s3, 0, 0x20000
	v_mov_b32_e32 v175, 0
	v_lshl_or_b32 v2, v3, 6, v2
	v_lshlrev_b32_e32 v3, 1, v16
	s_add_i32 s63, 0, 0x10000
	s_add_i32 s64, 0, 0x14000
	v_mov_b32_e32 v167, v161
	v_mov_b32_e32 v171, v161
	v_lshl_add_u32 v197, v196, 2, s3
	v_add_u32_e32 v198, s74, v7
	s_ashr_i32 s3, s2, 31
	v_add3_u32 v176, v2, v3, s8
	v_mov_b32_e32 v177, v175
	s_mov_b64 s[22:23], 0x100
	v_add_u32_e32 v199, s63, v195
	v_add_u32_e32 v200, s64, v195
	v_add_u32_e32 v201, 0, v5
	s_movk_i32 s65, 0x1c00
	s_mov_b32 s66, 0xc3e00000
	s_mov_b64 s[24:25], 0x1c000
	s_mov_b64 s[26:27], 0x8c000
	v_mov_b32_e32 v179, 0x41000000
	v_mov_b32_e32 v202, 0x43e00000
	s_barrier
	s_branch .LBB0_2085

; #define PG8_STAGE(bufoff, gbase, o0, o1) do { \
;         __builtin_amdgcn_global_load_lds((const unsigned*)((const char*)(gbase) + (o0)), (LAS unsigned*)(lds + (bufoff) + ldsw), 16, 0, 0); \
;         __builtin_amdgcn_global_load_lds((const unsigned*)((const char*)(gbase) + (o1)), (LAS unsigned*)(lds + (bufoff) + ldsw + 8192), 16, 0, 0); } while (0)
; #define PG8_LDA(dst, b, h) do { _Pragma("unroll") for (int m = 0; m < 4; ++m) _Pragma("unroll") for (int k = 0; k < 2; ++k) dst[m][k] = *(const LAS bf16x8*)(lds + PG8_SA(b, h) + aoff + m * 2048 + k * 1024); } while (0)
; #define PG8_LDB(dst, b, h) do { _Pragma("unroll") for (int n = 0; n < 2; ++n) _Pragma("unroll") for (int k = 0; k < 2; ++k) dst[n][k] = *(const LAS bf16x8*)(lds + PG8_SB(b, h) + boff + n * 2048 + k * 1024); } while (0)
; #define PG8_WAIT_V(n) asm volatile("s_waitcnt vmcnt(" #n ")" ::: "memory")
; #define PG8_WAIT_L(n) asm volatile("s_waitcnt lgkmcnt(" #n ")" ::: "memory")
; #define PG8_BAR __builtin_amdgcn_s_barrier()
; #define PG8_SCHED __builtin_amdgcn_sched_barrier(0)
; template <class Epi, class Sched, class Prob>
; __device__ __forceinline__ void gemm_phase(LAS unsigned char* lds, LAS unsigned char* lds_epi, const Prob g, const Sched& S, const Epi& E, int wid) {
;     ...
;         for (int t = 0; t < nt; t += 2) {
;             const bool last = (t == nt - 2);
;             const char* a1 = cA + (size_t)(t + 1) * kstep;
;             const char* a2 = last ? nA : cA + (size_t)(t + 2) * kstep; const char* b2 = last ? nB : cB + (size_t)(t + 2) * kstep;
;             const char* a3 = a2 + kstep; const char* b3 = b2 + kstep;
;             PG8_LDB(B0, 0, 0); PG8_LDB(B1, 0, 1); PG8_SCHED; PG8_LDA(At, 0, 0); PG8_STAGE(PG8_SA(1, 1), a1, cA10, cA11);
;             PG8_WAIT_V(8); PG8_WAIT_L(0); PG8_BAR; PG8_MMA(0, 0, At, B0); PG8_MMA(0, 1, At, B1); PG8_BAR; PG8_SCHED;
;             PG8_LDA(At, 0, 1); PG8_STAGE(PG8_SB(0, 0), b2, vB0, vB1); PG8_STAGE(PG8_SB(0, 1), b2 + hstepB, vB0, vB1); PG8_STAGE(PG8_SA(0, 0), a2, cA00, cA01);
;             PG8_WAIT_V(8); PG8_WAIT_L(0); PG8_BAR; PG8_MMA(1, 0, At, B0); PG8_MMA(1, 1, At, B1); PG8_BAR; PG8_SCHED;
.LBB0_2090:
	s_ashr_i32 s11, s10, 31
	s_lshl_b64 s[30:31], s[10:11], 19
	s_add_u32 s30, s51, s30
	s_addc_u32 s31, s52, s31
	s_and_b64 s[40:41], s[40:41], exec
	s_cselect_b32 s11, s31, s37
	s_cselect_b32 s29, s30, s36
	s_add_u32 s36, s36, 0x80
	v_mov_b32_e32 v32, 0
	s_addc_u32 s37, s37, 0
	v_lshl_add_u64 v[182:183], v[0:1], 0, s[22:23]
	s_mov_b32 s69, -2
	ds_read_b128 v[24:27], v199
	ds_read_b128 v[28:31], v199 offset:1024
	ds_read_b128 v[16:19], v199 offset:2048
	ds_read_b128 v[20:23], v199 offset:3072
	ds_read_b128 v[8:11], v200
	ds_read_b128 v[12:15], v200 offset:1024
	ds_read_b128 v[0:3], v200 offset:2048
	ds_read_b128 v[4:7], v200 offset:3072
	s_add_u32 s40, s36, 0x80
	s_addc_u32 s41, s37, 0
	s_cmp_eq_u32 s69, 12
	s_cselect_b64 vcc, -1, 0
	s_cselect_b32 s41, s11, s41
	s_cselect_b32 s40, s29, s40
	v_cndmask_b32_e32 v185, v183, v181, vcc
	v_cndmask_b32_e32 v184, v182, v180, vcc
	v_lshl_add_u64 v[228:229], s[36:37], 0, v[176:177]
	s_add_i32 m0, s35, 0xc000
	ds_read_b128 v[186:189], v201
	ds_read_b128 v[190:193], v201 offset:1024
	ds_read_b128 v[204:207], v201 offset:2048
	ds_read_b128 v[208:211], v201 offset:3072
	ds_read_b128 v[212:215], v201 offset:4096
	ds_read_b128 v[216:219], v201 offset:5120
	ds_read_b128 v[220:223], v201 offset:6144
	ds_read_b128 v[224:227], v201 offset:7168
	global_load_lds_dwordx4 v[228:229], off
	v_lshl_add_u64 v[228:229], s[36:37], 0, v[174:175]
	s_add_i32 m0, s35, 0xe000
	s_nop 0
	global_load_lds_dwordx4 v[228:229], off
	s_waitcnt vmcnt(16)
	s_waitcnt lgkmcnt(0)
	s_barrier
	s_setprio 1
	s_waitcnt lgkmcnt(0)
	v_mfma_f32_16x16x128_f8f6f4 v[156:159], v[24:31], v[186:193], 0
	v_mfma_f32_16x16x128_f8f6f4 v[152:155], v[16:23], v[186:193], 0
	v_mfma_f32_16x16x128_f8f6f4 v[140:143], v[24:31], v[204:211], 0
	v_mfma_f32_16x16x128_f8f6f4 v[136:139], v[16:23], v[204:211], 0
	v_mfma_f32_16x16x128_f8f6f4 v[124:127], v[24:31], v[212:219], 0
	v_mfma_f32_16x16x128_f8f6f4 v[120:123], v[16:23], v[212:219], 0
	v_mfma_f32_16x16x128_f8f6f4 v[108:111], v[24:31], v[220:227], 0
	v_mfma_f32_16x16x128_f8f6f4 v[104:107], v[16:23], v[220:227], 0
	s_setprio 0
	s_setprio 1
	v_mfma_f32_16x16x128_f8f6f4 v[148:151], v[8:15], v[186:193], 0
	v_mfma_f32_16x16x128_f8f6f4 v[144:147], v[0:7], v[186:193], 0
	v_mfma_f32_16x16x128_f8f6f4 v[132:135], v[8:15], v[204:211], 0
	v_mfma_f32_16x16x128_f8f6f4 v[128:131], v[0:7], v[204:211], 0
	v_mfma_f32_16x16x128_f8f6f4 v[116:119], v[8:15], v[212:219], 0
	v_mfma_f32_16x16x128_f8f6f4 v[112:115], v[0:7], v[212:219], 0
	v_mfma_f32_16x16x128_f8f6f4 v[100:103], v[8:15], v[220:227], 0
	v_mfma_f32_16x16x128_f8f6f4 v[96:99], v[0:7], v[220:227], 0
	s_setprio 0
	s_barrier
	s_add_i32 s70, s63, s97
	v_lshl_add_u64 v[186:187], v[184:185], 0, v[160:161]
	s_mov_b32 m0, s70
	ds_read_b128 v[204:207], v201 offset:16384
	ds_read_b128 v[208:211], v201 offset:17408
	ds_read_b128 v[212:215], v201 offset:18432
	ds_read_b128 v[216:219], v201 offset:19456
	ds_read_b128 v[220:223], v201 offset:20480
	ds_read_b128 v[224:227], v201 offset:21504
	ds_read_b128 v[228:231], v201 offset:22528
	ds_read_b128 v[232:235], v201 offset:23552
	global_load_lds_dwordx4 v[186:187], off
	v_lshl_add_u64 v[188:189], v[184:185], 0, v[162:163]
	s_add_i32 m0, s70, 0x2000
	v_lshl_add_u64 v[190:191], v[184:185], 0, s[12:13]
	s_add_i32 s70, s64, s97
	global_load_lds_dwordx4 v[188:189], off
	v_lshl_add_u64 v[192:193], v[190:191], 0, v[160:161]
	s_mov_b32 m0, s70
	v_lshl_add_u64 v[190:191], v[190:191], 0, v[162:163]
	global_load_lds_dwordx4 v[192:193], off
	s_add_i32 m0, s70, 0x2000
	v_lshl_add_u64 v[192:193], s[40:41], 0, v[168:169]
	global_load_lds_dwordx4 v[190:191], off
	v_lshl_add_u64 v[190:191], s[40:41], 0, v[164:165]
	s_mov_b32 m0, s35
	s_nop 0
	global_load_lds_dwordx4 v[190:191], off
	s_mov_b32 m0, s58
	s_nop 0
	global_load_lds_dwordx4 v[192:193], off
	s_waitcnt vmcnt(16)
	s_waitcnt lgkmcnt(0)
	s_barrier
	s_setprio 1
	s_waitcnt lgkmcnt(0)
	v_mfma_f32_16x16x128_f8f6f4 v[92:95], v[24:31], v[204:211], 0
	v_mfma_f32_16x16x128_f8f6f4 v[88:91], v[16:23], v[204:211], 0
	v_mfma_f32_16x16x128_f8f6f4 v[76:79], v[24:31], v[212:219], 0
	v_mfma_f32_16x16x128_f8f6f4 v[72:75], v[16:23], v[212:219], 0
	v_mfma_f32_16x16x128_f8f6f4 v[60:63], v[24:31], v[220:227], 0
	v_mfma_f32_16x16x128_f8f6f4 v[56:59], v[16:23], v[220:227], 0
	v_mfma_f32_16x16x128_f8f6f4 v[44:47], v[24:31], v[228:235], 0
	v_mfma_f32_16x16x128_f8f6f4 v[40:43], v[16:23], v[228:235], 0
	s_setprio 0
	s_setprio 1
	v_mfma_f32_16x16x128_f8f6f4 v[84:87], v[8:15], v[204:211], 0
	v_mfma_f32_16x16x128_f8f6f4 v[80:83], v[0:7], v[204:211], 0
	v_mfma_f32_16x16x128_f8f6f4 v[68:71], v[8:15], v[212:219], 0
	v_mfma_f32_16x16x128_f8f6f4 v[64:67], v[0:7], v[212:219], 0
	v_mfma_f32_16x16x128_f8f6f4 v[52:55], v[8:15], v[220:227], 0
	v_mfma_f32_16x16x128_f8f6f4 v[48:51], v[0:7], v[220:227], 0
	v_mfma_f32_16x16x128_f8f6f4 v[36:39], v[8:15], v[228:235], 0
	v_mfma_f32_16x16x128_f8f6f4 v[32:35], v[0:7], v[228:235], 0
	s_setprio 0
	s_barrier
; #define PG8_STAGE(bufoff, gbase, o0, o1) do { \
;         __builtin_amdgcn_global_load_lds((const unsigned*)((const char*)(gbase) + (o0)), (LAS unsigned*)(lds + (bufoff) + ldsw), 16, 0, 0); \
;         __builtin_amdgcn_global_load_lds((const unsigned*)((const char*)(gbase) + (o1)), (LAS unsigned*)(lds + (bufoff) + ldsw + 8192), 16, 0, 0); } while (0)
; #define PG8_LDA(dst, b, h) do { _Pragma("unroll") for (int m = 0; m < 4; ++m) _Pragma("unroll") for (int k = 0; k < 2; ++k) dst[m][k] = *(const LAS bf16x8*)(lds + PG8_SA(b, h) + aoff + m * 2048 + k * 1024); } while (0)
; #define PG8_LDB(dst, b, h) do { _Pragma("unroll") for (int n = 0; n < 2; ++n) _Pragma("unroll") for (int k = 0; k < 2; ++k) dst[n][k] = *(const LAS bf16x8*)(lds + PG8_SB(b, h) + boff + n * 2048 + k * 1024); } while (0)
; #define PG8_WAIT_V(n) asm volatile("s_waitcnt vmcnt(" #n ")" ::: "memory")
; #define PG8_WAIT_L(n) asm volatile("s_waitcnt lgkmcnt(" #n ")" ::: "memory")
; #define PG8_BAR __builtin_amdgcn_s_barrier()
; #define PG8_SCHED __builtin_amdgcn_sched_barrier(0)
; template <class Epi, class Sched, class Prob>
; __device__ __forceinline__ void gemm_phase(LAS unsigned char* lds, LAS unsigned char* lds_epi, const Prob g, const Sched& S, const Epi& E, int wid) {
;     ...
;             PG8_LDB(B0, 1, 0); PG8_LDB(B1, 1, 1); PG8_SCHED; PG8_LDA(At, 1, 0); PG8_STAGE(PG8_SA(0, 1), a2, cA10, cA11);
;             PG8_WAIT_V(8); PG8_WAIT_L(0); PG8_BAR; PG8_MMA(0, 0, At, B0); PG8_MMA(0, 1, At, B1); PG8_BAR; PG8_SCHED;
;             PG8_LDA(At, 1, 1); PG8_STAGE(PG8_SB(1, 0), b3, vB0, vB1); PG8_STAGE(PG8_SB(1, 1), b3 + hstepB, vB0, vB1); PG8_STAGE(PG8_SA(1, 0), a3, cA00, cA01);
;             PG8_WAIT_V(8); PG8_WAIT_L(0); PG8_BAR; PG8_MMA(1, 0, At, B0); PG8_MMA(1, 1, At, B1); PG8_BAR; PG8_SCHED;
;         }
	s_add_i32 s70, 0, 0x18000
	s_add_i32 s71, 0, 0x1c000
	v_add_u32_e32 v12, s70, v195
	v_add_u32_e32 v28, s71, v195
	ds_read_b128 v[0:3], v12
	ds_read_b128 v[4:7], v12 offset:1024
	ds_read_b128 v[8:11], v12 offset:2048
	ds_read_b128 v[12:15], v12 offset:3072
	ds_read_b128 v[16:19], v28
	ds_read_b128 v[20:23], v28 offset:1024
	ds_read_b128 v[24:27], v28 offset:2048
	ds_read_b128 v[28:31], v28 offset:3072
	s_mov_b32 m0, s59
	v_lshl_add_u64 v[236:237], s[40:41], 0, v[166:167]
	ds_read_b128 v[204:207], v201 offset:32768
	ds_read_b128 v[208:211], v201 offset:33792
	ds_read_b128 v[212:215], v201 offset:34816
	ds_read_b128 v[216:219], v201 offset:35840
	ds_read_b128 v[220:223], v201 offset:36864
	ds_read_b128 v[224:227], v201 offset:37888
	ds_read_b128 v[228:231], v201 offset:38912
	ds_read_b128 v[232:235], v201 offset:39936
	global_load_lds_dwordx4 v[236:237], off
	v_lshl_add_u64 v[236:237], s[40:41], 0, v[170:171]
	s_mov_b32 m0, s60
	s_nop 0
	global_load_lds_dwordx4 v[236:237], off
	s_waitcnt vmcnt(8)
	s_waitcnt lgkmcnt(0)
	s_barrier
	s_setprio 1
	s_waitcnt lgkmcnt(0)
	v_mfma_f32_16x16x128_f8f6f4 v[156:159], v[0:7], v[204:211], v[156:159]
	v_mfma_f32_16x16x128_f8f6f4 v[152:155], v[8:15], v[204:211], v[152:155]
	v_mfma_f32_16x16x128_f8f6f4 v[140:143], v[0:7], v[212:219], v[140:143]
	v_mfma_f32_16x16x128_f8f6f4 v[136:139], v[8:15], v[212:219], v[136:139]
	v_mfma_f32_16x16x128_f8f6f4 v[124:127], v[0:7], v[220:227], v[124:127]
	v_mfma_f32_16x16x128_f8f6f4 v[120:123], v[8:15], v[220:227], v[120:123]
	v_mfma_f32_16x16x128_f8f6f4 v[108:111], v[0:7], v[228:235], v[108:111]
	v_mfma_f32_16x16x128_f8f6f4 v[104:107], v[8:15], v[228:235], v[104:107]
	s_setprio 0
	s_setprio 1
	v_mfma_f32_16x16x128_f8f6f4 v[148:151], v[16:23], v[204:211], v[148:151]
	v_mfma_f32_16x16x128_f8f6f4 v[144:147], v[24:31], v[204:211], v[144:147]
	v_mfma_f32_16x16x128_f8f6f4 v[132:135], v[16:23], v[212:219], v[132:135]
	v_mfma_f32_16x16x128_f8f6f4 v[128:131], v[24:31], v[212:219], v[128:131]
	v_mfma_f32_16x16x128_f8f6f4 v[116:119], v[16:23], v[220:227], v[116:119]
	v_mfma_f32_16x16x128_f8f6f4 v[112:115], v[24:31], v[220:227], v[112:115]
	v_mfma_f32_16x16x128_f8f6f4 v[100:103], v[16:23], v[228:235], v[100:103]
	v_mfma_f32_16x16x128_f8f6f4 v[96:99], v[24:31], v[228:235], v[96:99]
	s_setprio 0
	s_barrier
	s_add_i32 s40, s70, s97
	v_lshl_add_u64 v[186:187], v[186:187], 0, s[18:19]
	s_mov_b32 m0, s40
	ds_read_b128 v[204:207], v201 offset:49152
	ds_read_b128 v[208:211], v201 offset:50176
	ds_read_b128 v[212:215], v201 offset:51200
	ds_read_b128 v[216:219], v201 offset:52224
	ds_read_b128 v[220:223], v201 offset:53248
	ds_read_b128 v[224:227], v201 offset:54272
	ds_read_b128 v[228:231], v201 offset:55296
	ds_read_b128 v[232:235], v201 offset:56320
	global_load_lds_dwordx4 v[186:187], off
	v_lshl_add_u64 v[186:187], v[188:189], 0, s[18:19]
	s_add_i32 m0, s40, 0x2000
	v_lshl_add_u64 v[184:185], v[184:185], 0, s[20:21]
	s_add_i32 s40, s71, s97
	global_load_lds_dwordx4 v[186:187], off
	v_lshl_add_u64 v[186:187], v[184:185], 0, v[160:161]
	s_mov_b32 m0, s40
	v_lshl_add_u64 v[184:185], v[184:185], 0, v[162:163]
	global_load_lds_dwordx4 v[186:187], off
	s_add_i32 m0, s40, 0x2000
	s_nop 0
	global_load_lds_dwordx4 v[184:185], off
	v_lshl_add_u64 v[184:185], v[190:191], 0, s[18:19]
	s_mov_b32 m0, s61
	s_nop 0
	global_load_lds_dwordx4 v[184:185], off
	v_lshl_add_u64 v[184:185], v[192:193], 0, s[18:19]
	s_mov_b32 m0, s62
	s_nop 0
	global_load_lds_dwordx4 v[184:185], off
	s_waitcnt vmcnt(8)
	s_waitcnt lgkmcnt(0)
	s_barrier
	s_setprio 1
	s_waitcnt lgkmcnt(0)
	v_mfma_f32_16x16x128_f8f6f4 v[92:95], v[0:7], v[204:211], v[92:95]
	v_mfma_f32_16x16x128_f8f6f4 v[88:91], v[8:15], v[204:211], v[88:91]
	v_mfma_f32_16x16x128_f8f6f4 v[76:79], v[0:7], v[212:219], v[76:79]
	v_mfma_f32_16x16x128_f8f6f4 v[72:75], v[8:15], v[212:219], v[72:75]
	v_mfma_f32_16x16x128_f8f6f4 v[60:63], v[0:7], v[220:227], v[60:63]
	v_mfma_f32_16x16x128_f8f6f4 v[56:59], v[8:15], v[220:227], v[56:59]
	v_mfma_f32_16x16x128_f8f6f4 v[44:47], v[0:7], v[228:235], v[44:47]
	v_mfma_f32_16x16x128_f8f6f4 v[40:43], v[8:15], v[228:235], v[40:43]
	s_setprio 0
	s_setprio 1
	v_mfma_f32_16x16x128_f8f6f4 v[84:87], v[16:23], v[204:211], v[84:87]
	v_mfma_f32_16x16x128_f8f6f4 v[80:83], v[24:31], v[204:211], v[80:83]
	v_mfma_f32_16x16x128_f8f6f4 v[68:71], v[16:23], v[212:219], v[68:71]
	v_mfma_f32_16x16x128_f8f6f4 v[64:67], v[24:31], v[212:219], v[64:67]
	v_mfma_f32_16x16x128_f8f6f4 v[52:55], v[16:23], v[220:227], v[52:55]
	v_mfma_f32_16x16x128_f8f6f4 v[48:51], v[24:31], v[220:227], v[48:51]
	v_mfma_f32_16x16x128_f8f6f4 v[36:39], v[16:23], v[228:235], v[36:39]
	v_mfma_f32_16x16x128_f8f6f4 v[32:35], v[24:31], v[228:235], v[32:35]
	s_setprio 0
	s_barrier
	s_add_i32 s69, s69, 2
	s_add_u32 s36, s36, 0x100
	s_addc_u32 s37, s37, 0
	s_cmp_gt_u32 s69, 13
	v_lshl_add_u64 v[182:183], v[182:183], 0, s[22:23]
